# topk index extraction: 30 sixteen-way compare/select chains replaced by an LDS read of the winning packed key + index decode
# baseline (speedup 1.0000x reference)
.LBB0_704:
	v_cndmask_b32_e64 v0, 0, 1, s[6:7]
	s_lshl_b32 s36, s8, 8
	v_cmp_ne_u32_e32 vcc, 1, v0
	v_lshl_add_u64 v[0:1], v[178:179], 0, s[36:37]
	global_load_dwordx4 v[44:47], v[0:1], off
	global_load_dwordx4 v[40:43], v[0:1], off offset:32
	global_load_dwordx4 v[36:39], v[0:1], off offset:64
	global_load_dwordx4 v[32:35], v[0:1], off offset:96
	global_load_dwordx4 v[28:31], v[0:1], off offset:128
	global_load_dwordx4 v[24:27], v[0:1], off offset:160
	global_load_dwordx4 v[20:23], v[0:1], off offset:192
	global_load_dwordx4 v[16:19], v[0:1], off offset:224
	v_lshl_or_b32 v180, s8, 7, v209
	v_ashrrev_i32_e32 v181, 31, v180
	v_lshlrev_b64 v[0:1], 8, v[180:181]
	v_lshl_add_u64 v[60:61], v[64:65], 0, v[0:1]
	global_load_dwordx4 v[0:3], v[60:61], off
	global_load_dwordx4 v[48:51], v[60:61], off offset:32
	global_load_dwordx4 v[52:55], v[60:61], off offset:64
	global_load_dwordx4 v[56:59], v[60:61], off offset:96
	s_nop 15
	s_nop 15
	s_waitcnt vmcnt(0)
	v_mfma_f32_32x32x16_bf16 v[0:15], v[0:3], v[44:47], 0
	v_mfma_f32_32x32x16_bf16 v[0:15], v[48:51], v[40:43], v[0:15]
	v_mfma_f32_32x32x16_bf16 v[0:15], v[52:55], v[36:39], v[0:15]
	v_mfma_f32_32x32x16_bf16 v[0:15], v[56:59], v[32:35], v[0:15]
	s_nop 15
	s_nop 15
	global_load_dwordx4 v[48:51], v[60:61], off offset:128
	global_load_dwordx4 v[52:55], v[60:61], off offset:160
	global_load_dwordx4 v[56:59], v[60:61], off offset:192
	s_nop 0
	global_load_dwordx4 v[60:63], v[60:61], off offset:224
	s_nop 15
	s_nop 15
	s_waitcnt vmcnt(3)
	v_mfma_f32_32x32x16_bf16 v[0:15], v[48:51], v[28:31], v[0:15]
	s_waitcnt vmcnt(2)
	v_mfma_f32_32x32x16_bf16 v[0:15], v[52:55], v[24:27], v[0:15]
	s_waitcnt vmcnt(1)
	v_mfma_f32_32x32x16_bf16 v[0:15], v[56:59], v[20:23], v[0:15]
	s_waitcnt vmcnt(0)
	v_mfma_f32_32x32x16_bf16 v[0:15], v[60:63], v[16:19], v[0:15]
	s_nop 15
	s_nop 15
	v_or_b32_e32 v49, 1, v66
	v_xor_b32_e32 v51, 0x7e, v66
	s_nop 9
	v_cmp_gt_i32_e64 s[6:7], 0, v1
	v_xor_b32_e32 v48, 0x7f, v66
	v_and_b32_e32 v1, 0xffffff80, v1
	v_cndmask_b32_e64 v49, v51, v49, s[6:7]
	v_cmp_gt_i32_e64 s[6:7], 0, v0
	v_and_b32_e32 v0, 0xffffff80, v0
	v_or_b32_e32 v210, v49, v1
	v_cndmask_b32_e64 v48, v48, v66, s[6:7]
	v_or_b32_e32 v211, v48, v0
	v_or_b32_e32 v48, 32, v180
	v_ashrrev_i32_e32 v49, 31, v48
	v_lshlrev_b64 v[48:49], 8, v[48:49]
	v_lshl_add_u64 v[182:183], v[64:65], 0, v[48:49]
	global_load_dwordx4 v[60:63], v[182:183], off
	global_load_dwordx4 v[56:59], v[182:183], off offset:32
	global_load_dwordx4 v[52:55], v[182:183], off offset:64
	global_load_dwordx4 v[48:51], v[182:183], off offset:96
	v_or_b32_e32 v1, 3, v66
	v_xor_b32_e32 v173, 0x7c, v66
	v_cmp_gt_i32_e64 s[6:7], 0, v3
	v_or_b32_e32 v0, 2, v66
	v_xor_b32_e32 v190, 0x7d, v66
	v_cndmask_b32_e64 v1, v173, v1, s[6:7]
	v_cmp_gt_i32_e64 s[6:7], 0, v2
	v_and_b32_e32 v3, 0xffffff80, v3
	v_and_b32_e32 v2, 0xffffff80, v2
	v_cndmask_b32_e64 v0, v190, v0, s[6:7]
	v_or_b32_e32 v173, v1, v3
	v_or_b32_e32 v1, 9, v66
	v_xor_b32_e32 v3, 0x76, v66
	v_cmp_gt_i32_e64 s[6:7], 0, v5
	v_or_b32_e32 v212, v0, v2
	v_or_b32_e32 v0, 8, v66
	v_cndmask_b32_e64 v1, v3, v1, s[6:7]
	v_xor_b32_e32 v2, 0x77, v66
	v_cmp_gt_i32_e64 s[6:7], 0, v4
	v_and_b32_e32 v3, 0xffffff80, v4
	s_nop 0
	v_cndmask_b32_e64 v0, v2, v0, s[6:7]
	v_and_b32_e32 v2, 0xffffff80, v5
	v_or_b32_e32 v213, v1, v2
	v_or_b32_e32 v214, v0, v3
	v_or_b32_e32 v1, 11, v66
	v_xor_b32_e32 v3, 0x74, v66
	v_cmp_gt_i32_e64 s[6:7], 0, v7
	v_or_b32_e32 v0, 10, v66
	v_xor_b32_e32 v2, 0x75, v66
	v_cndmask_b32_e64 v1, v3, v1, s[6:7]
	v_cmp_gt_i32_e64 s[6:7], 0, v6
	v_and_b32_e32 v3, 0xffffff80, v6
	s_nop 0
	v_cndmask_b32_e64 v0, v2, v0, s[6:7]
	v_and_b32_e32 v2, 0xffffff80, v7
	v_or_b32_e32 v215, v1, v2
	v_or_b32_e32 v216, v0, v3
	v_or_b32_e32 v1, 17, v66
	v_xor_b32_e32 v3, 0x6e, v66
	v_cmp_gt_i32_e64 s[6:7], 0, v9
	v_or_b32_e32 v0, 16, v66
	v_xor_b32_e32 v2, 0x6f, v66
	v_cndmask_b32_e64 v1, v3, v1, s[6:7]
	v_cmp_gt_i32_e64 s[6:7], 0, v8
	v_and_b32_e32 v3, 0xffffff80, v8
	s_nop 0
	v_cndmask_b32_e64 v0, v2, v0, s[6:7]
	v_and_b32_e32 v2, 0xffffff80, v9
	v_or_b32_e32 v217, v1, v2
	v_or_b32_e32 v218, v0, v3
	v_or_b32_e32 v1, 19, v66
	v_xor_b32_e32 v3, 0x6c, v66
	v_cmp_gt_i32_e64 s[6:7], 0, v11
	v_or_b32_e32 v0, 18, v66
	v_xor_b32_e32 v2, 0x6d, v66
	v_cndmask_b32_e64 v1, v3, v1, s[6:7]
	v_cmp_gt_i32_e64 s[6:7], 0, v10
	v_and_b32_e32 v3, 0xffffff80, v10
	s_nop 0
	v_cndmask_b32_e64 v0, v2, v0, s[6:7]
	v_and_b32_e32 v2, 0xffffff80, v11
	v_or_b32_e32 v219, v1, v2
	v_or_b32_e32 v220, v0, v3
	v_or_b32_e32 v1, 25, v66
	v_xor_b32_e32 v3, 0x66, v66
	v_cmp_gt_i32_e64 s[6:7], 0, v13
	v_or_b32_e32 v0, 24, v66
	v_xor_b32_e32 v2, 0x67, v66
	v_cndmask_b32_e64 v1, v3, v1, s[6:7]
	v_cmp_gt_i32_e64 s[6:7], 0, v12
	v_and_b32_e32 v3, 0xffffff80, v12
	s_nop 0
	v_cndmask_b32_e64 v0, v2, v0, s[6:7]
	v_and_b32_e32 v2, 0xffffff80, v13
	v_or_b32_e32 v221, v1, v2
	v_or_b32_e32 v1, 27, v66
	v_cmp_gt_i32_e64 s[6:7], 0, v15
	v_or_b32_e32 v222, v0, v3
	v_and_b32_e32 v2, 0xffffff80, v15
	v_cndmask_b32_e64 v0, v67, v1, s[6:7]
	v_cmp_gt_i32_e64 s[6:7], 0, v14
	v_and_b32_e32 v3, 0xffffff80, v14
	v_or_b32_e32 v223, v0, v2
	v_cndmask_b32_e64 v1, v70, v68, s[6:7]
	v_or_b32_e32 v224, v1, v3
	s_nop 15
	s_nop 15
	s_waitcnt vmcnt(3)
	v_mfma_f32_32x32x16_bf16 v[0:15], v[60:63], v[44:47], 0
	s_waitcnt vmcnt(2)
	v_mfma_f32_32x32x16_bf16 v[0:15], v[56:59], v[40:43], v[0:15]
	s_waitcnt vmcnt(1)
	v_mfma_f32_32x32x16_bf16 v[0:15], v[52:55], v[36:39], v[0:15]
	s_waitcnt vmcnt(0)
	v_mfma_f32_32x32x16_bf16 v[0:15], v[48:51], v[32:35], v[0:15]
	s_nop 15
	s_nop 15
	global_load_dwordx4 v[48:51], v[182:183], off offset:128
	global_load_dwordx4 v[52:55], v[182:183], off offset:160
	global_load_dwordx4 v[56:59], v[182:183], off offset:192
	global_load_dwordx4 v[60:63], v[182:183], off offset:224
	s_nop 15
	s_nop 15
	s_waitcnt vmcnt(3)
	v_mfma_f32_32x32x16_bf16 v[0:15], v[48:51], v[28:31], v[0:15]
	s_waitcnt vmcnt(2)
	v_mfma_f32_32x32x16_bf16 v[0:15], v[52:55], v[24:27], v[0:15]
	s_waitcnt vmcnt(1)
	v_mfma_f32_32x32x16_bf16 v[0:15], v[56:59], v[20:23], v[0:15]
	s_waitcnt vmcnt(0)
	v_mfma_f32_32x32x16_bf16 v[0:15], v[60:63], v[16:19], v[0:15]
	s_nop 15
	s_nop 15
	v_or_b32_e32 v48, 64, v180
	v_ashrrev_i32_e32 v49, 31, v48
	v_lshlrev_b64 v[48:49], 8, v[48:49]
	v_lshl_add_u64 v[182:183], v[64:65], 0, v[48:49]
	global_load_dwordx4 v[60:63], v[182:183], off
	global_load_dwordx4 v[56:59], v[182:183], off offset:32
	global_load_dwordx4 v[52:55], v[182:183], off offset:64
	global_load_dwordx4 v[48:51], v[182:183], off offset:96
	s_nop 3
	v_cmp_gt_i32_e64 s[6:7], 0, v1
	v_and_b32_e32 v1, 0xffffff80, v1
	s_nop 0
	v_cndmask_b32_e64 v181, v71, v69, s[6:7]
	v_cmp_gt_i32_e64 s[6:7], 0, v0
	v_and_b32_e32 v0, 0xffffff80, v0
	v_or_b32_e32 v225, v181, v1
	v_cndmask_b32_e64 v190, v74, v72, s[6:7]
	v_cmp_gt_i32_e64 s[6:7], 0, v3
	v_or_b32_e32 v226, v190, v0
	v_and_b32_e32 v3, 0xffffff80, v3
	v_cndmask_b32_e64 v0, v75, v73, s[6:7]
	v_cmp_gt_i32_e64 s[6:7], 0, v2
	v_and_b32_e32 v2, 0xffffff80, v2
	v_or_b32_e32 v227, v0, v3
	v_cndmask_b32_e64 v1, v78, v76, s[6:7]
	v_cmp_gt_i32_e64 s[6:7], 0, v5
	v_or_b32_e32 v228, v1, v2
	v_and_b32_e32 v2, 0xffffff80, v5
	v_cndmask_b32_e64 v0, v79, v77, s[6:7]
	v_cmp_gt_i32_e64 s[6:7], 0, v4
	v_and_b32_e32 v3, 0xffffff80, v4
	v_or_b32_e32 v229, v0, v2
	v_cndmask_b32_e64 v1, v82, v80, s[6:7]
	v_cmp_gt_i32_e64 s[6:7], 0, v7
	v_or_b32_e32 v230, v1, v3
	v_and_b32_e32 v2, 0xffffff80, v7
	v_cndmask_b32_e64 v0, v83, v81, s[6:7]
	v_cmp_gt_i32_e64 s[6:7], 0, v6
	v_and_b32_e32 v3, 0xffffff80, v6
	v_or_b32_e32 v231, v0, v2
	v_cndmask_b32_e64 v1, v86, v84, s[6:7]
	v_cmp_gt_i32_e64 s[6:7], 0, v9
	v_or_b32_e32 v232, v1, v3
	v_and_b32_e32 v2, 0xffffff80, v9
	v_cndmask_b32_e64 v0, v87, v85, s[6:7]
	v_cmp_gt_i32_e64 s[6:7], 0, v8
	v_and_b32_e32 v3, 0xffffff80, v8
	v_or_b32_e32 v233, v0, v2
	v_cndmask_b32_e64 v1, v90, v88, s[6:7]
	v_cmp_gt_i32_e64 s[6:7], 0, v11
	v_or_b32_e32 v234, v1, v3
	v_and_b32_e32 v2, 0xffffff80, v11
	v_cndmask_b32_e64 v0, v91, v89, s[6:7]
	v_cmp_gt_i32_e64 s[6:7], 0, v10
	v_and_b32_e32 v3, 0xffffff80, v10
	v_or_b32_e32 v235, v0, v2
	v_cndmask_b32_e64 v1, v94, v92, s[6:7]
	v_cmp_gt_i32_e64 s[6:7], 0, v13
	v_or_b32_e32 v236, v1, v3
	v_and_b32_e32 v2, 0xffffff80, v13
	v_cndmask_b32_e64 v0, v95, v93, s[6:7]
	v_cmp_gt_i32_e64 s[6:7], 0, v12
	v_and_b32_e32 v3, 0xffffff80, v12
	v_or_b32_e32 v237, v0, v2
	v_cndmask_b32_e64 v1, v98, v96, s[6:7]
	v_cmp_gt_i32_e64 s[6:7], 0, v15
	v_or_b32_e32 v238, v1, v3
	v_and_b32_e32 v2, 0xffffff80, v15
	v_cndmask_b32_e64 v0, v99, v97, s[6:7]
	v_cmp_gt_i32_e64 s[6:7], 0, v14
	v_and_b32_e32 v3, 0xffffff80, v14
	v_or_b32_e32 v239, v0, v2
	v_cndmask_b32_e64 v1, v102, v100, s[6:7]
	v_or_b32_e32 v240, v1, v3
	s_nop 15
	s_nop 15
	s_waitcnt vmcnt(3)
	v_mfma_f32_32x32x16_bf16 v[0:15], v[60:63], v[44:47], 0
	s_waitcnt vmcnt(2)
	v_mfma_f32_32x32x16_bf16 v[0:15], v[56:59], v[40:43], v[0:15]
	s_waitcnt vmcnt(1)
	v_mfma_f32_32x32x16_bf16 v[0:15], v[52:55], v[36:39], v[0:15]
	s_waitcnt vmcnt(0)
	v_mfma_f32_32x32x16_bf16 v[0:15], v[48:51], v[32:35], v[0:15]
	s_nop 15
	s_nop 15
	global_load_dwordx4 v[48:51], v[182:183], off offset:128
	global_load_dwordx4 v[52:55], v[182:183], off offset:160
	global_load_dwordx4 v[56:59], v[182:183], off offset:192
	global_load_dwordx4 v[60:63], v[182:183], off offset:224
	s_nop 15
	s_nop 15
	s_waitcnt vmcnt(3)
	v_mfma_f32_32x32x16_bf16 v[0:15], v[48:51], v[28:31], v[0:15]
	s_waitcnt vmcnt(2)
	v_mfma_f32_32x32x16_bf16 v[0:15], v[52:55], v[24:27], v[0:15]
	s_waitcnt vmcnt(1)
	v_mfma_f32_32x32x16_bf16 v[0:15], v[56:59], v[20:23], v[0:15]
	s_waitcnt vmcnt(0)
	v_mfma_f32_32x32x16_bf16 v[0:15], v[60:63], v[16:19], v[0:15]
	s_nop 15
	s_nop 15
	v_or_b32_e32 v48, 0x60, v180
	v_ashrrev_i32_e32 v49, 31, v48
	v_lshlrev_b64 v[48:49], 8, v[48:49]
	v_lshl_add_u64 v[180:181], v[64:65], 0, v[48:49]
	global_load_dwordx4 v[60:63], v[180:181], off
	global_load_dwordx4 v[56:59], v[180:181], off offset:32
	global_load_dwordx4 v[52:55], v[180:181], off offset:64
	global_load_dwordx4 v[48:51], v[180:181], off offset:96
	s_nop 3
	v_cmp_gt_i32_e64 s[6:7], 0, v1
	v_and_b32_e32 v1, 0xffffff80, v1
	s_nop 0
	v_cndmask_b32_e64 v182, v103, v101, s[6:7]
	v_cmp_gt_i32_e64 s[6:7], 0, v0
	v_and_b32_e32 v0, 0xffffff80, v0
	v_or_b32_e32 v182, v182, v1
	v_cndmask_b32_e64 v183, v106, v104, s[6:7]
	v_cmp_gt_i32_e64 s[6:7], 0, v3
	v_or_b32_e32 v183, v183, v0
	v_and_b32_e32 v3, 0xffffff80, v3
	v_cndmask_b32_e64 v0, v107, v105, s[6:7]
	v_cmp_gt_i32_e64 s[6:7], 0, v2
	v_and_b32_e32 v2, 0xffffff80, v2
	v_or_b32_e32 v241, v0, v3
	v_cndmask_b32_e64 v1, v110, v108, s[6:7]
	v_cmp_gt_i32_e64 s[6:7], 0, v5
	v_or_b32_e32 v242, v1, v2
	v_and_b32_e32 v2, 0xffffff80, v5
	v_cndmask_b32_e64 v0, v111, v109, s[6:7]
	v_cmp_gt_i32_e64 s[6:7], 0, v4
	v_and_b32_e32 v3, 0xffffff80, v4
	v_or_b32_e32 v243, v0, v2
	v_cndmask_b32_e64 v1, v114, v112, s[6:7]
	v_cmp_gt_i32_e64 s[6:7], 0, v7
	v_or_b32_e32 v244, v1, v3
	v_and_b32_e32 v2, 0xffffff80, v7
	v_cndmask_b32_e64 v0, v115, v113, s[6:7]
	v_cmp_gt_i32_e64 s[6:7], 0, v6
	v_and_b32_e32 v3, 0xffffff80, v6
	v_or_b32_e32 v245, v0, v2
	v_cndmask_b32_e64 v1, v118, v116, s[6:7]
	v_cmp_gt_i32_e64 s[6:7], 0, v9
	v_or_b32_e32 v246, v1, v3
	v_and_b32_e32 v2, 0xffffff80, v9
	v_cndmask_b32_e64 v0, v119, v117, s[6:7]
	v_cmp_gt_i32_e64 s[6:7], 0, v8
	v_and_b32_e32 v3, 0xffffff80, v8
	v_or_b32_e32 v247, v0, v2
	v_cndmask_b32_e64 v1, v122, v120, s[6:7]
	v_cmp_gt_i32_e64 s[6:7], 0, v11
	v_or_b32_e32 v248, v1, v3
	v_and_b32_e32 v2, 0xffffff80, v11
	v_cndmask_b32_e64 v0, v123, v121, s[6:7]
	v_cmp_gt_i32_e64 s[6:7], 0, v10
	v_and_b32_e32 v3, 0xffffff80, v10
	v_or_b32_e32 v249, v0, v2
	v_cndmask_b32_e64 v1, v126, v124, s[6:7]
	v_cmp_gt_i32_e64 s[6:7], 0, v13
	v_or_b32_e32 v250, v1, v3
	v_and_b32_e32 v2, 0xffffff80, v13
	v_cndmask_b32_e64 v0, v127, v125, s[6:7]
	v_cmp_gt_i32_e64 s[6:7], 0, v12
	v_and_b32_e32 v3, 0xffffff80, v12
	v_or_b32_e32 v251, v0, v2
	v_cndmask_b32_e64 v1, v130, v128, s[6:7]
	v_cmp_gt_i32_e64 s[6:7], 0, v15
	v_or_b32_e32 v252, v1, v3
	v_and_b32_e32 v2, 0xffffff80, v15
	v_cndmask_b32_e64 v0, v131, v129, s[6:7]
	v_cmp_gt_i32_e64 s[6:7], 0, v14
	v_and_b32_e32 v3, 0xffffff80, v14
	v_or_b32_e32 v190, v0, v2
	v_cndmask_b32_e64 v1, v134, v132, s[6:7]
	v_or_b32_e32 v195, v1, v3
	s_nop 15
	s_nop 15
	s_waitcnt vmcnt(3)
	v_mfma_f32_32x32x16_bf16 v[0:15], v[60:63], v[44:47], 0
	s_waitcnt vmcnt(2)
	v_mfma_f32_32x32x16_bf16 v[0:15], v[56:59], v[40:43], v[0:15]
	s_waitcnt vmcnt(1)
	v_mfma_f32_32x32x16_bf16 v[0:15], v[52:55], v[36:39], v[0:15]
	s_waitcnt vmcnt(0)
	v_mfma_f32_32x32x16_bf16 v[0:15], v[48:51], v[32:35], v[0:15]
	s_nop 15
	s_nop 15
	global_load_dwordx4 v[32:35], v[180:181], off offset:128
	global_load_dwordx4 v[36:39], v[180:181], off offset:160
	global_load_dwordx4 v[40:43], v[180:181], off offset:192
	global_load_dwordx4 v[44:47], v[180:181], off offset:224
	s_nop 15
	s_nop 15
	s_waitcnt vmcnt(3)
	v_mfma_f32_32x32x16_bf16 v[0:15], v[32:35], v[28:31], v[0:15]
	s_waitcnt vmcnt(2)
	v_mfma_f32_32x32x16_bf16 v[0:15], v[36:39], v[24:27], v[0:15]
	s_waitcnt vmcnt(1)
	v_mfma_f32_32x32x16_bf16 v[0:15], v[40:43], v[20:23], v[0:15]
	s_waitcnt vmcnt(0)
	v_mfma_f32_32x32x16_bf16 v[0:15], v[44:47], v[16:19], v[0:15]
	s_nop 15
	s_nop 15
	s_nop 11
	v_cmp_gt_i32_e64 s[6:7], 0, v1
	v_and_b32_e32 v1, 0xffffff80, v1
	v_and_b32_e32 v18, 0xffffff80, v0
	v_cndmask_b32_e64 v16, v135, v133, s[6:7]
	v_cmp_gt_i32_e64 s[6:7], 0, v0
	v_or_b32_e32 v0, v16, v1
	s_nop 0
	v_cndmask_b32_e64 v17, v138, v136, s[6:7]
	v_cmp_gt_i32_e64 s[6:7], 0, v3
	v_or_b32_e32 v1, v17, v18
	v_and_b32_e32 v3, 0xffffff80, v3
	v_cndmask_b32_e64 v16, v139, v137, s[6:7]
	v_cmp_gt_i32_e64 s[6:7], 0, v2
	v_and_b32_e32 v18, 0xffffff80, v2
	v_or_b32_e32 v2, v16, v3
	v_cndmask_b32_e64 v17, v142, v140, s[6:7]
	v_cmp_gt_i32_e64 s[6:7], 0, v5
	v_or_b32_e32 v3, v17, v18
	v_and_b32_e32 v5, 0xffffff80, v5
	v_cndmask_b32_e64 v16, v143, v141, s[6:7]
	v_cmp_gt_i32_e64 s[6:7], 0, v4
	v_and_b32_e32 v18, 0xffffff80, v4
	v_or_b32_e32 v4, v16, v5
	v_cndmask_b32_e64 v17, v154, v152, s[6:7]
	v_cmp_gt_i32_e64 s[6:7], 0, v7
	v_or_b32_e32 v5, v17, v18
	v_and_b32_e32 v7, 0xffffff80, v7
	v_cndmask_b32_e64 v16, v155, v153, s[6:7]
	v_cmp_gt_i32_e64 s[6:7], 0, v6
	v_and_b32_e32 v18, 0xffffff80, v6
	v_or_b32_e32 v6, v16, v7
	v_cndmask_b32_e64 v17, v158, v156, s[6:7]
	v_cmp_gt_i32_e64 s[6:7], 0, v9
	v_or_b32_e32 v7, v17, v18
	v_and_b32_e32 v9, 0xffffff80, v9
	v_cndmask_b32_e64 v16, v159, v157, s[6:7]
	v_cmp_gt_i32_e64 s[6:7], 0, v8
	v_and_b32_e32 v18, 0xffffff80, v8
	v_or_b32_e32 v8, v16, v9
	v_cndmask_b32_e64 v17, v162, v160, s[6:7]
	v_cmp_gt_i32_e64 s[6:7], 0, v11
	v_or_b32_e32 v9, v17, v18
	v_and_b32_e32 v11, 0xffffff80, v11
	v_cndmask_b32_e64 v16, v163, v161, s[6:7]
	v_cmp_gt_i32_e64 s[6:7], 0, v10
	v_and_b32_e32 v18, 0xffffff80, v10
	v_or_b32_e32 v10, v16, v11
	v_cndmask_b32_e64 v17, v166, v164, s[6:7]
	v_cmp_gt_i32_e64 s[6:7], 0, v13
	v_or_b32_e32 v11, v17, v18
	v_and_b32_e32 v13, 0xffffff80, v13
	v_cndmask_b32_e64 v16, v167, v165, s[6:7]
	v_cmp_gt_i32_e64 s[6:7], 0, v12
	v_and_b32_e32 v18, 0xffffff80, v12
	v_or_b32_e32 v12, v16, v13
	v_cndmask_b32_e64 v17, v170, v168, s[6:7]
	v_cmp_gt_i32_e64 s[6:7], 0, v15
	v_or_b32_e32 v16, v17, v18
	v_and_b32_e32 v15, 0xffffff80, v15
	v_cndmask_b32_e64 v13, v171, v169, s[6:7]
	v_cmp_gt_i32_e64 s[6:7], 0, v14
	v_and_b32_e32 v14, 0xffffff80, v14
	v_or_b32_e32 v25, v13, v15
	v_cndmask_b32_e64 v17, v174, v172, s[6:7]
	v_or_b32_e32 v28, v17, v14
	v_max_f32_e32 v13, v211, v210
	v_min_f32_e32 v14, v211, v210
	v_min_f32_e32 v15, v212, v173
	v_max_f32_e32 v17, v212, v173
	v_max_f32_e32 v18, v214, v213
	v_min_f32_e32 v19, v214, v213
	v_min_f32_e32 v20, v216, v215
	v_max_f32_e32 v21, v216, v215
	v_max_f32_e32 v22, v218, v217
	v_min_f32_e32 v23, v218, v217
	v_min_f32_e32 v24, v220, v219
	v_max_f32_e32 v26, v220, v219
	v_max_f32_e32 v27, v222, v221
	v_min_f32_e32 v29, v222, v221
	v_min_f32_e32 v30, v224, v223
	v_max_f32_e32 v31, v224, v223
	v_max_f32_e32 v32, v13, v15
	v_min_f32_e32 v13, v13, v15
	v_max_f32_e32 v15, v14, v17
	v_min_f32_e32 v14, v14, v17
	v_min_f32_e32 v17, v18, v20
	v_max_f32_e32 v18, v18, v20
	v_min_f32_e32 v20, v19, v21
	v_max_f32_e32 v19, v19, v21
	v_max_f32_e32 v21, v22, v24
	v_min_f32_e32 v22, v22, v24
	v_max_f32_e32 v24, v23, v26
	v_min_f32_e32 v23, v23, v26
	v_min_f32_e32 v26, v27, v30
	v_max_f32_e32 v27, v27, v30
	v_min_f32_e32 v30, v29, v31
	v_max_f32_e32 v29, v29, v31
	v_max_f32_e32 v31, v32, v15
	v_min_f32_e32 v15, v32, v15
	v_max_f32_e32 v32, v13, v14
	v_min_f32_e32 v13, v13, v14
	v_min_f32_e32 v14, v17, v20
	v_max_f32_e32 v17, v17, v20
	v_min_f32_e32 v20, v18, v19
	v_max_f32_e32 v18, v18, v19
	v_max_f32_e32 v19, v21, v24
	v_min_f32_e32 v21, v21, v24
	v_max_f32_e32 v24, v22, v23
	v_min_f32_e32 v22, v22, v23
	v_min_f32_e32 v23, v26, v30
	v_max_f32_e32 v26, v26, v30
	v_min_f32_e32 v30, v27, v29
	v_max_f32_e32 v27, v27, v29
	v_max_f32_e32 v29, v31, v14
	v_min_f32_e32 v14, v31, v14
	v_max_f32_e32 v31, v15, v17
	v_min_f32_e32 v15, v15, v17
	v_max_f32_e32 v17, v32, v20
	v_min_f32_e32 v20, v32, v20
	v_max_f32_e32 v32, v13, v18
	v_min_f32_e32 v13, v13, v18
	v_min_f32_e32 v18, v19, v23
	v_max_f32_e32 v19, v19, v23
	v_min_f32_e32 v23, v21, v26
	v_max_f32_e32 v21, v21, v26
	v_min_f32_e32 v26, v24, v30
	v_max_f32_e32 v24, v24, v30
	v_min_f32_e32 v30, v22, v27
	v_max_f32_e32 v22, v22, v27
	v_max_f32_e32 v27, v29, v17
	v_min_f32_e32 v17, v29, v17
	v_max_f32_e32 v29, v31, v32
	v_min_f32_e32 v31, v31, v32
	v_max_f32_e32 v32, v14, v20
	v_min_f32_e32 v14, v14, v20
	v_max_f32_e32 v20, v15, v13
	v_min_f32_e32 v13, v15, v13
	v_min_f32_e32 v15, v18, v26
	v_max_f32_e32 v18, v18, v26
	v_min_f32_e32 v26, v23, v30
	v_max_f32_e32 v23, v23, v30
	v_min_f32_e32 v30, v19, v24
	v_max_f32_e32 v19, v19, v24
	v_min_f32_e32 v24, v21, v22
	v_max_f32_e32 v21, v21, v22
	v_max_f32_e32 v22, v27, v29
	v_min_f32_e32 v27, v27, v29
	v_max_f32_e32 v29, v17, v31
	v_min_f32_e32 v17, v17, v31
	v_max_f32_e32 v31, v32, v20
	v_min_f32_e32 v20, v32, v20
	v_max_f32_e32 v32, v14, v13
	v_min_f32_e32 v13, v14, v13
	v_min_f32_e32 v14, v15, v26
	v_max_f32_e32 v15, v15, v26
	v_min_f32_e32 v26, v18, v23
	v_max_f32_e32 v18, v18, v23
	v_min_f32_e32 v23, v30, v24
	v_max_f32_e32 v24, v30, v24
	v_min_f32_e32 v30, v19, v21
	v_max_f32_e32 v19, v19, v21
	v_max_f32_e32 v21, v22, v14
	v_min_f32_e32 v14, v22, v14
	v_max_f32_e32 v22, v27, v15
	v_min_f32_e32 v15, v27, v15
	v_max_f32_e32 v27, v29, v26
	v_min_f32_e32 v26, v29, v26
	v_max_f32_e32 v29, v17, v18
	v_min_f32_e32 v17, v17, v18
	v_max_f32_e32 v18, v31, v23
	v_min_f32_e32 v23, v31, v23
	v_max_f32_e32 v31, v20, v24
	v_min_f32_e32 v20, v20, v24
	v_max_f32_e32 v24, v32, v30
	v_min_f32_e32 v30, v32, v30
	v_max_f32_e32 v32, v13, v19
	v_min_f32_e32 v13, v13, v19
	v_max_f32_e32 v19, v21, v18
	v_min_f32_e32 v18, v21, v18
	v_max_f32_e32 v21, v22, v31
	v_min_f32_e32 v22, v22, v31
	v_max_f32_e32 v31, v27, v24
	v_min_f32_e32 v24, v27, v24
	v_max_f32_e32 v27, v29, v32
	v_min_f32_e32 v29, v29, v32
	v_max_f32_e32 v32, v14, v23
	v_min_f32_e32 v14, v14, v23
	v_max_f32_e32 v23, v15, v20
	v_min_f32_e32 v15, v15, v20
	v_max_f32_e32 v20, v26, v30
	v_min_f32_e32 v26, v26, v30
	v_max_f32_e32 v30, v17, v13
	v_min_f32_e32 v13, v17, v13
	v_max_f32_e32 v17, v19, v31
	v_min_f32_e32 v19, v19, v31
	v_max_f32_e32 v33, v21, v27
	v_min_f32_e32 v21, v21, v27
	v_max_f32_e32 v34, v18, v24
	v_min_f32_e32 v18, v18, v24
	v_max_f32_e32 v24, v22, v29
	v_min_f32_e32 v22, v22, v29
	v_max_f32_e32 v35, v32, v20
	v_min_f32_e32 v32, v32, v20
	v_max_f32_e32 v20, v23, v30
	v_min_f32_e32 v36, v23, v30
	v_max_f32_e32 v37, v14, v26
	v_min_f32_e32 v38, v14, v26
	v_max_f32_e32 v14, v15, v13
	v_min_f32_e32 v13, v15, v13
	v_max_f32_e32 v31, v17, v33
	v_min_f32_e32 v29, v17, v33
	v_max_f32_e32 v30, v19, v21
	v_min_f32_e32 v26, v19, v21
	v_max_f32_e32 v27, v34, v24
	v_min_f32_e32 v23, v34, v24
	v_max_f32_e32 v24, v18, v22
	v_min_f32_e32 v21, v18, v22
	v_max_f32_e32 v22, v35, v20
	v_min_f32_e32 v19, v35, v20
	v_max_f32_e32 v20, v32, v36
	v_min_f32_e32 v17, v32, v36
	v_max_f32_e32 v18, v37, v14
	v_min_f32_e32 v14, v37, v14
	v_max_f32_e32 v15, v38, v13
	v_min_f32_e32 v13, v38, v13
	v_max_f32_e32 v32, v226, v225
	v_min_f32_e32 v33, v226, v225
	v_min_f32_e32 v34, v228, v227
	v_max_f32_e32 v35, v228, v227
	v_max_f32_e32 v36, v230, v229
	v_min_f32_e32 v37, v230, v229
	v_min_f32_e32 v38, v232, v231
	v_max_f32_e32 v39, v232, v231
	v_max_f32_e32 v40, v234, v233
	v_min_f32_e32 v41, v234, v233
	v_min_f32_e32 v42, v236, v235
	v_max_f32_e32 v43, v236, v235
	v_max_f32_e32 v44, v238, v237
	v_min_f32_e32 v45, v238, v237
	v_min_f32_e32 v46, v240, v239
	v_max_f32_e32 v47, v240, v239
	v_max_f32_e32 v48, v32, v34
	v_min_f32_e32 v32, v32, v34
	v_max_f32_e32 v34, v33, v35
	v_min_f32_e32 v33, v33, v35
	v_min_f32_e32 v35, v36, v38
	v_max_f32_e32 v36, v36, v38
	v_min_f32_e32 v38, v37, v39
	v_max_f32_e32 v37, v37, v39
	v_max_f32_e32 v39, v40, v42
	v_min_f32_e32 v40, v40, v42
	v_max_f32_e32 v42, v41, v43
	v_min_f32_e32 v41, v41, v43
	v_min_f32_e32 v43, v44, v46
	v_max_f32_e32 v44, v44, v46
	v_min_f32_e32 v46, v45, v47
	v_max_f32_e32 v45, v45, v47
	v_max_f32_e32 v47, v48, v34
	v_min_f32_e32 v34, v48, v34
	v_max_f32_e32 v48, v32, v33
	v_min_f32_e32 v32, v32, v33
	v_min_f32_e32 v33, v35, v38
	v_max_f32_e32 v35, v35, v38
	v_min_f32_e32 v38, v36, v37
	v_max_f32_e32 v36, v36, v37
	v_max_f32_e32 v37, v39, v42
	v_min_f32_e32 v39, v39, v42
	v_max_f32_e32 v42, v40, v41
	v_min_f32_e32 v40, v40, v41
	v_min_f32_e32 v41, v43, v46
	v_max_f32_e32 v43, v43, v46
	v_min_f32_e32 v46, v44, v45
	v_max_f32_e32 v44, v44, v45
	v_max_f32_e32 v45, v47, v33
	v_min_f32_e32 v33, v47, v33
	v_max_f32_e32 v47, v34, v35
	v_min_f32_e32 v34, v34, v35
	v_max_f32_e32 v35, v48, v38
	v_min_f32_e32 v38, v48, v38
	v_max_f32_e32 v48, v32, v36
	v_min_f32_e32 v32, v32, v36
	v_min_f32_e32 v36, v37, v41
	v_max_f32_e32 v37, v37, v41
	v_min_f32_e32 v41, v39, v43
	v_max_f32_e32 v39, v39, v43
	v_min_f32_e32 v43, v42, v46
	v_max_f32_e32 v42, v42, v46
	v_min_f32_e32 v46, v40, v44
	v_max_f32_e32 v40, v40, v44
	v_max_f32_e32 v44, v45, v35
	v_min_f32_e32 v35, v45, v35
	v_max_f32_e32 v45, v47, v48
	v_min_f32_e32 v47, v47, v48
	v_max_f32_e32 v48, v33, v38
	v_min_f32_e32 v33, v33, v38
	v_max_f32_e32 v38, v34, v32
	v_min_f32_e32 v32, v34, v32
	v_min_f32_e32 v34, v36, v43
	v_max_f32_e32 v36, v36, v43
	v_min_f32_e32 v43, v41, v46
	v_max_f32_e32 v41, v41, v46
	v_min_f32_e32 v46, v37, v42
	v_max_f32_e32 v37, v37, v42
	v_min_f32_e32 v42, v39, v40
	v_max_f32_e32 v39, v39, v40
	v_max_f32_e32 v40, v44, v45
	v_min_f32_e32 v44, v44, v45
	v_max_f32_e32 v45, v35, v47
	v_min_f32_e32 v35, v35, v47
	v_max_f32_e32 v47, v48, v38
	v_min_f32_e32 v38, v48, v38
	v_max_f32_e32 v48, v33, v32
	v_min_f32_e32 v32, v33, v32
	v_min_f32_e32 v33, v34, v43
	v_max_f32_e32 v34, v34, v43
	v_min_f32_e32 v43, v36, v41
	v_max_f32_e32 v36, v36, v41
	v_min_f32_e32 v41, v46, v42
	v_max_f32_e32 v42, v46, v42
	v_min_f32_e32 v46, v37, v39
	v_max_f32_e32 v37, v37, v39
	v_max_f32_e32 v39, v40, v33
	v_min_f32_e32 v33, v40, v33
	v_max_f32_e32 v40, v44, v34
	v_min_f32_e32 v34, v44, v34
	v_max_f32_e32 v44, v45, v43
	v_min_f32_e32 v43, v45, v43
	v_max_f32_e32 v45, v35, v36
	v_min_f32_e32 v35, v35, v36
	v_max_f32_e32 v36, v47, v41
	v_min_f32_e32 v41, v47, v41
	v_max_f32_e32 v47, v38, v42
	v_min_f32_e32 v38, v38, v42
	v_max_f32_e32 v42, v48, v46
	v_min_f32_e32 v46, v48, v46
	v_max_f32_e32 v48, v32, v37
	v_min_f32_e32 v32, v32, v37
	v_max_f32_e32 v37, v39, v36
	v_min_f32_e32 v36, v39, v36
	v_max_f32_e32 v39, v40, v47
	v_min_f32_e32 v40, v40, v47
	v_max_f32_e32 v47, v44, v42
	v_min_f32_e32 v42, v44, v42
	v_max_f32_e32 v44, v45, v48
	v_min_f32_e32 v45, v45, v48
	v_max_f32_e32 v48, v33, v41
	v_min_f32_e32 v33, v33, v41
	v_max_f32_e32 v41, v34, v38
	v_min_f32_e32 v34, v34, v38
	v_max_f32_e32 v38, v43, v46
	v_min_f32_e32 v43, v43, v46
	v_max_f32_e32 v46, v35, v32
	v_min_f32_e32 v32, v35, v32
	v_max_f32_e32 v35, v37, v47
	v_min_f32_e32 v37, v37, v47
	v_max_f32_e32 v47, v39, v44
	v_min_f32_e32 v39, v39, v44
	v_max_f32_e32 v44, v36, v42
	v_min_f32_e32 v42, v36, v42
	v_max_f32_e32 v49, v40, v45
	v_min_f32_e32 v40, v40, v45
	v_max_f32_e32 v45, v48, v38
	v_min_f32_e32 v48, v48, v38
	v_max_f32_e32 v50, v41, v46
	v_min_f32_e32 v41, v41, v46
	v_max_f32_e32 v46, v33, v43
	v_min_f32_e32 v43, v33, v43
	v_max_f32_e32 v51, v34, v32
	v_min_f32_e32 v52, v34, v32
	v_max_f32_e32 v32, v35, v47
	v_min_f32_e32 v33, v35, v47
	v_max_f32_e32 v34, v37, v39
	v_min_f32_e32 v35, v37, v39
	v_max_f32_e32 v36, v44, v49
	v_min_f32_e32 v37, v44, v49
	v_max_f32_e32 v38, v42, v40
	v_min_f32_e32 v39, v42, v40
	v_max_f32_e32 v40, v45, v50
	v_min_f32_e32 v42, v45, v50
	v_max_f32_e32 v44, v48, v41
	v_min_f32_e32 v41, v48, v41
	v_max_f32_e32 v45, v46, v51
	v_min_f32_e32 v46, v46, v51
	v_max_f32_e32 v47, v43, v52
	v_min_f32_e32 v43, v43, v52
	v_max_f32_e32 v48, v183, v182
	v_min_f32_e32 v49, v183, v182
	v_min_f32_e32 v50, v242, v241
	v_max_f32_e32 v51, v242, v241
	v_max_f32_e32 v52, v244, v243
	v_min_f32_e32 v53, v244, v243
	v_min_f32_e32 v54, v246, v245
	v_max_f32_e32 v55, v246, v245
	v_max_f32_e32 v56, v248, v247
	v_min_f32_e32 v57, v248, v247
	v_min_f32_e32 v58, v250, v249
	v_max_f32_e32 v59, v250, v249
	v_max_f32_e32 v60, v252, v251
	v_min_f32_e32 v61, v252, v251
	v_min_f32_e32 v62, v195, v190
	v_max_f32_e32 v63, v195, v190
	v_max_f32_e32 v173, v48, v50
	v_min_f32_e32 v48, v48, v50
	v_max_f32_e32 v50, v49, v51
	v_min_f32_e32 v49, v49, v51
	v_min_f32_e32 v51, v52, v54
	v_max_f32_e32 v52, v52, v54
	v_min_f32_e32 v54, v53, v55
	v_max_f32_e32 v53, v53, v55
	v_max_f32_e32 v55, v56, v58
	v_min_f32_e32 v56, v56, v58
	v_max_f32_e32 v58, v57, v59
	v_min_f32_e32 v57, v57, v59
	v_min_f32_e32 v59, v60, v62
	v_max_f32_e32 v60, v60, v62
	v_min_f32_e32 v62, v61, v63
	v_max_f32_e32 v61, v61, v63
	v_max_f32_e32 v63, v173, v50
	v_min_f32_e32 v50, v173, v50
	v_max_f32_e32 v173, v48, v49
	v_min_f32_e32 v48, v48, v49
	v_min_f32_e32 v49, v51, v54
	v_max_f32_e32 v51, v51, v54
	v_min_f32_e32 v54, v52, v53
	v_max_f32_e32 v52, v52, v53
	v_max_f32_e32 v53, v55, v58
	v_min_f32_e32 v55, v55, v58
	v_max_f32_e32 v58, v56, v57
	v_min_f32_e32 v56, v56, v57
	v_min_f32_e32 v57, v59, v62
	v_max_f32_e32 v59, v59, v62
	v_min_f32_e32 v62, v60, v61
	v_max_f32_e32 v60, v60, v61
	v_max_f32_e32 v61, v63, v49
	v_min_f32_e32 v49, v63, v49
	v_max_f32_e32 v63, v50, v51
	v_min_f32_e32 v50, v50, v51
	v_max_f32_e32 v51, v173, v54
	v_min_f32_e32 v54, v173, v54
	v_max_f32_e32 v173, v48, v52
	v_min_f32_e32 v48, v48, v52
	v_min_f32_e32 v52, v53, v57
	v_max_f32_e32 v53, v53, v57
	v_min_f32_e32 v57, v55, v59
	v_max_f32_e32 v55, v55, v59
	v_min_f32_e32 v59, v58, v62
	v_max_f32_e32 v58, v58, v62
	v_min_f32_e32 v62, v56, v60
	v_max_f32_e32 v56, v56, v60
	v_max_f32_e32 v60, v61, v51
	v_min_f32_e32 v51, v61, v51
	v_max_f32_e32 v61, v63, v173
	v_min_f32_e32 v63, v63, v173
	v_max_f32_e32 v173, v49, v54
	v_min_f32_e32 v49, v49, v54
	v_max_f32_e32 v54, v50, v48
	v_min_f32_e32 v48, v50, v48
	v_min_f32_e32 v50, v52, v59
	v_max_f32_e32 v52, v52, v59
	v_min_f32_e32 v59, v57, v62
	v_max_f32_e32 v57, v57, v62
	v_min_f32_e32 v62, v53, v58
	v_max_f32_e32 v53, v53, v58
	v_min_f32_e32 v58, v55, v56
	v_max_f32_e32 v55, v55, v56
	v_max_f32_e32 v56, v60, v61
	v_min_f32_e32 v60, v60, v61
	v_max_f32_e32 v61, v51, v63
	v_min_f32_e32 v51, v51, v63
	v_max_f32_e32 v63, v173, v54
	v_min_f32_e32 v54, v173, v54
	v_max_f32_e32 v173, v49, v48
	v_min_f32_e32 v48, v49, v48
	v_min_f32_e32 v49, v50, v59
	v_max_f32_e32 v50, v50, v59
	v_min_f32_e32 v59, v52, v57
	v_max_f32_e32 v52, v52, v57
	v_min_f32_e32 v57, v62, v58
	v_max_f32_e32 v58, v62, v58
	v_min_f32_e32 v62, v53, v55
	v_max_f32_e32 v53, v53, v55
	v_max_f32_e32 v55, v56, v49
	v_min_f32_e32 v49, v56, v49
	v_max_f32_e32 v56, v60, v50
	v_min_f32_e32 v50, v60, v50
	v_max_f32_e32 v60, v61, v59
	v_min_f32_e32 v59, v61, v59
	v_max_f32_e32 v61, v51, v52
	v_min_f32_e32 v51, v51, v52
	v_max_f32_e32 v52, v63, v57
	v_min_f32_e32 v57, v63, v57
	v_max_f32_e32 v63, v54, v58
	v_min_f32_e32 v54, v54, v58
	v_max_f32_e32 v58, v173, v62
	v_min_f32_e32 v62, v173, v62
	v_max_f32_e32 v173, v48, v53
	v_min_f32_e32 v48, v48, v53
	v_max_f32_e32 v53, v55, v52
	v_min_f32_e32 v52, v55, v52
	v_max_f32_e32 v55, v56, v63
	v_min_f32_e32 v56, v56, v63
	v_max_f32_e32 v63, v60, v58
	v_min_f32_e32 v58, v60, v58
	v_max_f32_e32 v60, v61, v173
	v_min_f32_e32 v61, v61, v173
	v_max_f32_e32 v173, v49, v57
	v_min_f32_e32 v49, v49, v57
	v_max_f32_e32 v57, v50, v54
	v_min_f32_e32 v50, v50, v54
	v_max_f32_e32 v54, v59, v62
	v_min_f32_e32 v59, v59, v62
	v_max_f32_e32 v62, v51, v48
	v_min_f32_e32 v48, v51, v48
	v_max_f32_e32 v51, v53, v63
	v_min_f32_e32 v53, v53, v63
	v_max_f32_e32 v63, v55, v60
	v_min_f32_e32 v55, v55, v60
	v_max_f32_e32 v60, v52, v58
	v_min_f32_e32 v52, v52, v58
	v_max_f32_e32 v58, v56, v61
	v_min_f32_e32 v56, v56, v61
	v_max_f32_e32 v61, v173, v54
	v_min_f32_e32 v54, v173, v54
	v_max_f32_e32 v173, v57, v62
	v_min_f32_e32 v57, v57, v62
	v_max_f32_e32 v62, v49, v59
	v_min_f32_e32 v49, v49, v59
	v_max_f32_e32 v59, v50, v48
	v_min_f32_e32 v48, v50, v48
	v_max_f32_e32 v50, v51, v63
	v_min_f32_e32 v51, v51, v63
	v_max_f32_e32 v63, v53, v55
	v_min_f32_e32 v53, v53, v55
	v_max_f32_e32 v55, v60, v58
	v_min_f32_e32 v58, v60, v58
	v_max_f32_e32 v60, v52, v56
	v_min_f32_e32 v52, v52, v56
	v_max_f32_e32 v56, v61, v173
	v_min_f32_e32 v61, v61, v173
	v_max_f32_e32 v173, v54, v57
	v_min_f32_e32 v54, v54, v57
	v_max_f32_e32 v57, v62, v59
	v_min_f32_e32 v59, v62, v59
	v_max_f32_e32 v62, v49, v48
	v_min_f32_e32 v48, v49, v48
	v_max_f32_e32 v49, v1, v0
	v_min_f32_e32 v0, v1, v0
	v_min_f32_e32 v1, v3, v2
	v_max_f32_e32 v2, v3, v2
	v_max_f32_e32 v3, v5, v4
	v_min_f32_e32 v4, v5, v4
	v_min_f32_e32 v5, v7, v6
	v_max_f32_e32 v6, v7, v6
	v_max_f32_e32 v7, v9, v8
	v_min_f32_e32 v8, v9, v8
	v_min_f32_e32 v9, v11, v10
	v_max_f32_e32 v10, v11, v10
	v_max_f32_e32 v11, v16, v12
	v_min_f32_e32 v12, v16, v12
	v_min_f32_e32 v16, v28, v25
	v_max_f32_e32 v25, v28, v25
	v_max_f32_e32 v28, v49, v1
	v_min_f32_e32 v1, v49, v1
	v_max_f32_e32 v49, v0, v2
	v_min_f32_e32 v0, v0, v2
	v_min_f32_e32 v2, v3, v5
	v_max_f32_e32 v3, v3, v5
	v_min_f32_e32 v5, v4, v6
	v_max_f32_e32 v4, v4, v6
	v_max_f32_e32 v6, v7, v9
	v_min_f32_e32 v7, v7, v9
	v_max_f32_e32 v9, v8, v10
	v_min_f32_e32 v8, v8, v10
	v_min_f32_e32 v10, v11, v16
	v_max_f32_e32 v11, v11, v16
	v_min_f32_e32 v16, v12, v25
	v_max_f32_e32 v12, v12, v25
	v_max_f32_e32 v25, v28, v49
	v_min_f32_e32 v28, v28, v49
	v_max_f32_e32 v49, v1, v0
	v_min_f32_e32 v0, v1, v0
	v_min_f32_e32 v1, v2, v5
	v_max_f32_e32 v2, v2, v5
	v_min_f32_e32 v5, v3, v4
	v_max_f32_e32 v3, v3, v4
	v_max_f32_e32 v4, v6, v9
	v_min_f32_e32 v6, v6, v9
	v_max_f32_e32 v9, v7, v8
	v_min_f32_e32 v7, v7, v8
	v_min_f32_e32 v8, v10, v16
	v_max_f32_e32 v10, v10, v16
	v_min_f32_e32 v16, v11, v12
	v_max_f32_e32 v11, v11, v12
	v_max_f32_e32 v12, v25, v1
	v_min_f32_e32 v1, v25, v1
	v_max_f32_e32 v25, v28, v2
	v_min_f32_e32 v2, v28, v2
	v_max_f32_e32 v28, v49, v5
	v_min_f32_e32 v5, v49, v5
	v_max_f32_e32 v49, v0, v3
	v_min_f32_e32 v0, v0, v3
	v_min_f32_e32 v3, v4, v8
	v_max_f32_e32 v4, v4, v8
	v_min_f32_e32 v8, v6, v10
	v_max_f32_e32 v6, v6, v10
	v_min_f32_e32 v10, v9, v16
	v_max_f32_e32 v9, v9, v16
	v_min_f32_e32 v16, v7, v11
	v_max_f32_e32 v7, v7, v11
	v_max_f32_e32 v11, v12, v28
	v_min_f32_e32 v12, v12, v28
	v_max_f32_e32 v28, v25, v49
	v_min_f32_e32 v25, v25, v49
	v_max_f32_e32 v49, v1, v5
	v_min_f32_e32 v1, v1, v5
	v_max_f32_e32 v5, v2, v0
	v_min_f32_e32 v0, v2, v0
	v_min_f32_e32 v2, v3, v10
	v_max_f32_e32 v3, v3, v10
	v_min_f32_e32 v10, v8, v16
	v_max_f32_e32 v8, v8, v16
	v_min_f32_e32 v16, v4, v9
	v_max_f32_e32 v4, v4, v9
	v_min_f32_e32 v9, v6, v7
	v_max_f32_e32 v6, v6, v7
	v_max_f32_e32 v7, v11, v28
	v_min_f32_e32 v11, v11, v28
	v_max_f32_e32 v28, v12, v25
	v_min_f32_e32 v12, v12, v25
	v_max_f32_e32 v25, v49, v5
	v_min_f32_e32 v5, v49, v5
	v_max_f32_e32 v49, v1, v0
	v_min_f32_e32 v0, v1, v0
	v_min_f32_e32 v1, v2, v10
	v_max_f32_e32 v2, v2, v10
	v_min_f32_e32 v10, v3, v8
	v_max_f32_e32 v3, v3, v8
	v_min_f32_e32 v8, v16, v9
	v_max_f32_e32 v9, v16, v9
	v_min_f32_e32 v16, v4, v6
	v_max_f32_e32 v4, v4, v6
	v_max_f32_e32 v6, v7, v1
	v_min_f32_e32 v1, v7, v1
	v_max_f32_e32 v7, v11, v2
	v_min_f32_e32 v2, v11, v2
	v_max_f32_e32 v11, v28, v10
	v_min_f32_e32 v10, v28, v10
	v_max_f32_e32 v28, v12, v3
	v_min_f32_e32 v3, v12, v3
	v_max_f32_e32 v12, v25, v8
	v_min_f32_e32 v8, v25, v8
	v_max_f32_e32 v25, v5, v9
	v_min_f32_e32 v5, v5, v9
	v_max_f32_e32 v9, v49, v16
	v_min_f32_e32 v16, v49, v16
	v_max_f32_e32 v49, v0, v4
	v_min_f32_e32 v0, v0, v4
	v_max_f32_e32 v4, v6, v12
	v_min_f32_e32 v6, v6, v12
	v_max_f32_e32 v12, v7, v25
	v_min_f32_e32 v7, v7, v25
	v_max_f32_e32 v25, v11, v9
	v_min_f32_e32 v9, v11, v9
	v_max_f32_e32 v11, v28, v49
	v_min_f32_e32 v28, v28, v49
	v_max_f32_e32 v49, v1, v8
	v_min_f32_e32 v1, v1, v8
	v_max_f32_e32 v8, v2, v5
	v_min_f32_e32 v2, v2, v5
	v_max_f32_e32 v5, v10, v16
	v_min_f32_e32 v10, v10, v16
	v_max_f32_e32 v16, v3, v0
	v_min_f32_e32 v0, v3, v0
	v_max_f32_e32 v3, v4, v25
	v_min_f32_e32 v4, v4, v25
	v_max_f32_e32 v25, v12, v11
	v_min_f32_e32 v11, v12, v11
	v_max_f32_e32 v12, v6, v9
	v_min_f32_e32 v6, v6, v9
	v_max_f32_e32 v9, v7, v28
	v_min_f32_e32 v7, v7, v28
	v_max_f32_e32 v28, v49, v5
	v_min_f32_e32 v5, v49, v5
	v_max_f32_e32 v49, v8, v16
	v_min_f32_e32 v8, v8, v16
	v_max_f32_e32 v16, v1, v10
	v_min_f32_e32 v1, v1, v10
	v_max_f32_e32 v10, v2, v0
	v_min_f32_e32 v0, v2, v0
	v_max_f32_e32 v2, v3, v25
	v_min_f32_e32 v3, v3, v25
	v_max_f32_e32 v25, v4, v11
	v_min_f32_e32 v4, v4, v11
	v_max_f32_e32 v11, v12, v9
	v_min_f32_e32 v9, v12, v9
	v_max_f32_e32 v12, v6, v7
	v_min_f32_e32 v6, v6, v7
	v_max_f32_e32 v7, v28, v49
	v_min_f32_e32 v28, v28, v49
	v_max_f32_e32 v49, v5, v8
	v_min_f32_e32 v5, v5, v8
	v_max_f32_e32 v8, v16, v10
	v_min_f32_e32 v10, v16, v10
	v_max_f32_e32 v16, v1, v0
	v_min_f32_e32 v0, v1, v0
	v_max_f32_e32 v1, v31, v43
	v_max_f32_e32 v29, v29, v47
	v_max_f32_e32 v30, v30, v46
	v_max_f32_e32 v26, v26, v45
	v_max_f32_e32 v27, v27, v41
	v_max_f32_e32 v23, v23, v44
	v_max_f32_e32 v24, v24, v42
	v_max_f32_e32 v21, v21, v40
	v_max_f32_e32 v22, v22, v39
	v_max_f32_e32 v19, v19, v38
	v_max_f32_e32 v20, v20, v37
	v_max_f32_e32 v17, v17, v36
	v_max_f32_e32 v18, v18, v35
	v_max_f32_e32 v14, v14, v34
	v_max_f32_e32 v15, v15, v33
	v_max_f32_e32 v13, v13, v32
	v_max_f32_e32 v31, v1, v22
	v_min_f32_e32 v1, v1, v22
	v_max_f32_e32 v22, v29, v19
	v_min_f32_e32 v19, v29, v19
	v_max_f32_e32 v29, v30, v20
	v_min_f32_e32 v20, v30, v20
	v_max_f32_e32 v30, v26, v17
	v_min_f32_e32 v17, v26, v17
	v_max_f32_e32 v26, v27, v18
	v_min_f32_e32 v18, v27, v18
	v_max_f32_e32 v27, v23, v14
	v_min_f32_e32 v14, v23, v14
	v_max_f32_e32 v23, v24, v15
	v_min_f32_e32 v15, v24, v15
	v_max_f32_e32 v24, v21, v13
	v_min_f32_e32 v13, v21, v13
	v_max_f32_e32 v21, v31, v26
	v_min_f32_e32 v26, v31, v26
	v_max_f32_e32 v31, v22, v27
	v_min_f32_e32 v22, v22, v27
	v_max_f32_e32 v27, v29, v23
	v_min_f32_e32 v23, v29, v23
	v_max_f32_e32 v29, v30, v24
	v_min_f32_e32 v24, v30, v24
	v_max_f32_e32 v30, v1, v18
	v_min_f32_e32 v1, v1, v18
	v_max_f32_e32 v18, v19, v14
	v_min_f32_e32 v14, v19, v14
	v_max_f32_e32 v19, v20, v15
	v_min_f32_e32 v15, v20, v15
	v_max_f32_e32 v20, v17, v13
	v_min_f32_e32 v13, v17, v13
	v_max_f32_e32 v17, v21, v27
	v_min_f32_e32 v21, v21, v27
	v_max_f32_e32 v27, v31, v29
	v_min_f32_e32 v29, v31, v29
	v_max_f32_e32 v31, v26, v23
	v_min_f32_e32 v23, v26, v23
	v_max_f32_e32 v26, v22, v24
	v_min_f32_e32 v22, v22, v24
	v_max_f32_e32 v24, v30, v19
	v_min_f32_e32 v19, v30, v19
	v_max_f32_e32 v30, v18, v20
	v_min_f32_e32 v18, v18, v20
	v_max_f32_e32 v20, v1, v15
	v_min_f32_e32 v1, v1, v15
	v_max_f32_e32 v15, v14, v13
	v_min_f32_e32 v13, v14, v13
	v_max_f32_e32 v14, v17, v27
	v_min_f32_e32 v17, v17, v27
	v_max_f32_e32 v27, v21, v29
	v_min_f32_e32 v21, v21, v29
	v_max_f32_e32 v29, v31, v26
	v_min_f32_e32 v26, v31, v26
	v_max_f32_e32 v31, v23, v22
	v_min_f32_e32 v22, v23, v22
	v_max_f32_e32 v23, v24, v30
	v_min_f32_e32 v24, v24, v30
	v_max_f32_e32 v30, v19, v18
	v_min_f32_e32 v18, v19, v18
	v_max_f32_e32 v19, v20, v15
	v_min_f32_e32 v15, v20, v15
	v_max_f32_e32 v20, v1, v13
	v_min_f32_e32 v1, v1, v13
	v_max_f32_e32 v0, v50, v0
	v_max_f32_e32 v13, v51, v16
	v_max_f32_e32 v10, v63, v10
	v_max_f32_e32 v8, v53, v8
	v_max_f32_e32 v5, v55, v5
	v_max_f32_e32 v16, v58, v49
	v_max_f32_e32 v28, v60, v28
	v_max_f32_e32 v7, v52, v7
	v_max_f32_e32 v6, v56, v6
	v_max_f32_e32 v12, v61, v12
	v_max_f32_e32 v9, v173, v9
	v_max_f32_e32 v11, v54, v11
	v_max_f32_e32 v4, v57, v4
	v_max_f32_e32 v25, v59, v25
	v_max_f32_e32 v3, v62, v3
	v_max_f32_e32 v2, v48, v2
	v_max_f32_e32 v32, v0, v6
	v_min_f32_e32 v0, v0, v6
	v_max_f32_e32 v6, v13, v12
	v_min_f32_e32 v12, v13, v12
	v_max_f32_e32 v13, v10, v9
	v_min_f32_e32 v9, v10, v9
	v_max_f32_e32 v10, v8, v11
	v_min_f32_e32 v8, v8, v11
	v_max_f32_e32 v11, v5, v4
	v_min_f32_e32 v4, v5, v4
	v_max_f32_e32 v5, v16, v25
	v_min_f32_e32 v16, v16, v25
	v_max_f32_e32 v25, v28, v3
	v_min_f32_e32 v3, v28, v3
	v_max_f32_e32 v28, v7, v2
	v_min_f32_e32 v2, v7, v2
	v_max_f32_e32 v7, v32, v11
	v_min_f32_e32 v11, v32, v11
	v_max_f32_e32 v32, v6, v5
	v_min_f32_e32 v5, v6, v5
	v_max_f32_e32 v6, v13, v25
	v_min_f32_e32 v13, v13, v25
	v_max_f32_e32 v25, v10, v28
	v_min_f32_e32 v10, v10, v28
	v_max_f32_e32 v28, v0, v4
	v_min_f32_e32 v0, v0, v4
	v_max_f32_e32 v4, v12, v16
	v_min_f32_e32 v12, v12, v16
	v_max_f32_e32 v16, v9, v3
	v_min_f32_e32 v3, v9, v3
	v_max_f32_e32 v9, v8, v2
	v_min_f32_e32 v2, v8, v2
	v_max_f32_e32 v8, v7, v6
	v_min_f32_e32 v6, v7, v6
	v_max_f32_e32 v7, v32, v25
	v_min_f32_e32 v25, v32, v25
	v_max_f32_e32 v32, v11, v13
	v_min_f32_e32 v11, v11, v13
	v_max_f32_e32 v13, v5, v10
	v_min_f32_e32 v5, v5, v10
	v_max_f32_e32 v10, v28, v16
	v_min_f32_e32 v16, v28, v16
	v_max_f32_e32 v28, v4, v9
	v_min_f32_e32 v4, v4, v9
	v_max_f32_e32 v9, v0, v3
	v_min_f32_e32 v0, v0, v3
	v_max_f32_e32 v3, v12, v2
	v_min_f32_e32 v2, v12, v2
	v_max_f32_e32 v12, v8, v7
	v_min_f32_e32 v7, v8, v7
	v_max_f32_e32 v8, v6, v25
	v_min_f32_e32 v6, v6, v25
	v_max_f32_e32 v25, v32, v13
	v_min_f32_e32 v13, v32, v13
	v_max_f32_e32 v32, v11, v5
	v_min_f32_e32 v5, v11, v5
	v_max_f32_e32 v11, v10, v28
	v_min_f32_e32 v10, v10, v28
	v_max_f32_e32 v28, v16, v4
	v_min_f32_e32 v4, v16, v4
	v_max_f32_e32 v16, v9, v3
	v_min_f32_e32 v3, v9, v3
	v_max_f32_e32 v9, v0, v2
	v_min_f32_e32 v0, v0, v2
	v_max_f32_e32 v0, v14, v0
	v_max_f32_e32 v2, v17, v9
	v_max_f32_e32 v3, v27, v3
	v_max_f32_e32 v9, v21, v16
	v_max_f32_e32 v4, v29, v4
	v_max_f32_e32 v14, v26, v28
	v_max_f32_e32 v10, v31, v10
	v_max_f32_e32 v11, v22, v11
	v_max_f32_e32 v5, v23, v5
	v_max_f32_e32 v16, v24, v32
	v_max_f32_e32 v13, v30, v13
	v_max_f32_e32 v17, v18, v25
	v_max_f32_e32 v6, v19, v6
	v_max_f32_e32 v8, v15, v8
	v_max_f32_e32 v7, v20, v7
	v_max_f32_e32 v1, v1, v12
	v_max_f32_e32 v12, v0, v5
	v_min_f32_e32 v0, v0, v5
	v_max_f32_e32 v5, v2, v16
	v_min_f32_e32 v2, v2, v16
	v_max_f32_e32 v15, v3, v13
	v_min_f32_e32 v3, v3, v13
	v_max_f32_e32 v13, v9, v17
	v_min_f32_e32 v9, v9, v17
	v_max_f32_e32 v16, v4, v6
	v_min_f32_e32 v4, v4, v6
	v_max_f32_e32 v6, v14, v8
	v_min_f32_e32 v8, v14, v8
	v_max_f32_e32 v14, v10, v7
	v_min_f32_e32 v7, v10, v7
	v_max_f32_e32 v10, v11, v1
	v_min_f32_e32 v1, v11, v1
	v_max_f32_e32 v11, v12, v16
	v_min_f32_e32 v12, v12, v16
	v_max_f32_e32 v16, v5, v6
	v_min_f32_e32 v5, v5, v6
	v_max_f32_e32 v6, v15, v14
	v_min_f32_e32 v14, v15, v14
	v_max_f32_e32 v15, v13, v10
	v_min_f32_e32 v10, v13, v10
	v_max_f32_e32 v13, v0, v4
	v_min_f32_e32 v0, v0, v4
	v_max_f32_e32 v4, v2, v8
	v_min_f32_e32 v2, v2, v8
	v_max_f32_e32 v8, v3, v7
	v_min_f32_e32 v3, v3, v7
	v_max_f32_e32 v7, v9, v1
	v_min_f32_e32 v1, v9, v1
	v_max_f32_e32 v9, v11, v6
	v_min_f32_e32 v6, v11, v6
	v_max_f32_e32 v11, v16, v15
	v_min_f32_e32 v15, v16, v15
	v_max_f32_e32 v16, v12, v14
	v_min_f32_e32 v12, v12, v14
	v_max_f32_e32 v14, v5, v10
	v_min_f32_e32 v5, v5, v10
	v_max_f32_e32 v10, v13, v8
	v_min_f32_e32 v8, v13, v8
	v_max_f32_e32 v13, v4, v7
	v_min_f32_e32 v4, v4, v7
	v_max_f32_e32 v7, v0, v3
	v_min_f32_e32 v0, v0, v3
	v_max_f32_e32 v3, v2, v1
	v_min_f32_e32 v1, v2, v1
	v_max_f32_e32 v2, v9, v11
	v_min_f32_e32 v9, v9, v11
	v_max_f32_e32 v11, v6, v15
	v_min_f32_e32 v6, v6, v15
	v_max_f32_e32 v15, v16, v14
	v_min_f32_e32 v14, v16, v14
	v_max_f32_e32 v16, v12, v5
	v_min_f32_e32 v5, v12, v5
	v_max_f32_e32 v12, v10, v13
	v_min_f32_e32 v10, v10, v13
	v_max_f32_e32 v13, v8, v4
	v_min_f32_e32 v4, v8, v4
	v_max_f32_e32 v8, v7, v3
	v_min_f32_e32 v3, v7, v3
	v_max_f32_e32 v7, v0, v1
	v_min_f32_e32 v0, v0, v1
	ds_bpermute_b32 v27, v184, v0
	ds_bpermute_b32 v29, v184, v7
	ds_bpermute_b32 v31, v184, v3
	ds_bpermute_b32 v30, v184, v8
	ds_bpermute_b32 v28, v184, v4
	ds_bpermute_b32 v26, v184, v13
	s_waitcnt lgkmcnt(5)
	ds_bpermute_b32 v1, v184, v2
	ds_bpermute_b32 v25, v184, v10
	v_max_f32_e32 v2, v2, v27
	s_waitcnt lgkmcnt(6)
	ds_bpermute_b32 v17, v184, v9
	ds_bpermute_b32 v24, v184, v12
	v_max_f32_e32 v9, v9, v29
	s_waitcnt lgkmcnt(7)
	ds_bpermute_b32 v18, v184, v11
	ds_bpermute_b32 v23, v184, v5
	v_max_f32_e32 v11, v11, v31
	s_waitcnt lgkmcnt(8)
	ds_bpermute_b32 v19, v184, v6
	ds_bpermute_b32 v22, v184, v16
	v_max_f32_e32 v6, v6, v30
	s_waitcnt lgkmcnt(9)
	ds_bpermute_b32 v20, v184, v15
	ds_bpermute_b32 v21, v184, v14
	v_max_f32_e32 v15, v15, v28
	s_waitcnt lgkmcnt(10)
	v_max_f32_e32 v14, v14, v26
	s_waitcnt lgkmcnt(8)
	v_max_f32_e32 v16, v16, v25
	s_waitcnt lgkmcnt(6)
	v_max_f32_e32 v5, v5, v24
	s_waitcnt lgkmcnt(4)
	v_max_f32_e32 v12, v12, v23
	s_waitcnt lgkmcnt(2)
	v_max_f32_e32 v10, v10, v22
	s_waitcnt lgkmcnt(0)
	v_max_f32_e32 v13, v13, v21
	v_max_f32_e32 v4, v4, v20
	v_max_f32_e32 v8, v8, v19
	v_max_f32_e32 v3, v3, v18
	v_max_f32_e32 v7, v7, v17
	v_max_f32_e32 v0, v0, v1
	v_max_f32_e32 v1, v2, v12
	v_min_f32_e32 v2, v2, v12
	v_max_f32_e32 v12, v9, v10
	v_min_f32_e32 v9, v9, v10
	v_max_f32_e32 v10, v11, v13
	v_min_f32_e32 v11, v11, v13
	v_max_f32_e32 v13, v6, v4
	v_min_f32_e32 v4, v6, v4
	v_max_f32_e32 v6, v15, v8
	v_min_f32_e32 v8, v15, v8
	v_max_f32_e32 v15, v14, v3
	v_min_f32_e32 v3, v14, v3
	v_max_f32_e32 v14, v16, v7
	v_min_f32_e32 v7, v16, v7
	v_max_f32_e32 v16, v5, v0
	v_min_f32_e32 v0, v5, v0
	v_max_f32_e32 v5, v1, v6
	v_min_f32_e32 v1, v1, v6
	v_max_f32_e32 v6, v12, v15
	v_min_f32_e32 v12, v12, v15
	v_max_f32_e32 v15, v10, v14
	v_min_f32_e32 v10, v10, v14
	v_max_f32_e32 v14, v13, v16
	v_min_f32_e32 v13, v13, v16
	v_max_f32_e32 v16, v2, v8
	v_min_f32_e32 v2, v2, v8
	v_max_f32_e32 v8, v9, v3
	v_min_f32_e32 v3, v9, v3
	v_max_f32_e32 v9, v11, v7
	v_min_f32_e32 v7, v11, v7
	v_max_f32_e32 v11, v4, v0
	v_min_f32_e32 v0, v4, v0
	v_max_f32_e32 v4, v5, v15
	v_min_f32_e32 v5, v5, v15
	v_max_f32_e32 v15, v6, v14
	v_min_f32_e32 v6, v6, v14
	v_max_f32_e32 v14, v1, v10
	v_min_f32_e32 v1, v1, v10
	v_max_f32_e32 v10, v12, v13
	v_min_f32_e32 v12, v12, v13
	v_max_f32_e32 v13, v16, v9
	v_min_f32_e32 v9, v16, v9
	v_max_f32_e32 v16, v8, v11
	v_min_f32_e32 v8, v8, v11
	v_max_f32_e32 v11, v2, v7
	v_min_f32_e32 v2, v2, v7
	v_max_f32_e32 v7, v3, v0
	v_min_f32_e32 v0, v3, v0
	v_max_f32_e32 v3, v4, v15
	v_min_f32_e32 v4, v4, v15
	v_max_f32_e32 v15, v5, v6
	v_min_f32_e32 v5, v5, v6
	v_max_f32_e32 v6, v14, v10
	v_min_f32_e32 v10, v14, v10
	v_max_f32_e32 v14, v1, v12
	v_min_f32_e32 v1, v1, v12
	v_max_f32_e32 v12, v13, v16
	v_min_f32_e32 v13, v13, v16
	v_max_f32_e32 v16, v9, v8
	v_min_f32_e32 v8, v9, v8
	v_max_f32_e32 v9, v11, v7
	v_min_f32_e32 v7, v11, v7
	v_max_f32_e32 v11, v2, v0
	v_min_f32_e32 v0, v2, v0
	v_lshl_add_u32 v2, s8, 12, v207
	ds_write2st64_b32 v2, v3, v4 offset1:1
	ds_write2st64_b32 v2, v15, v5 offset0:2 offset1:3
	ds_write2st64_b32 v2, v6, v10 offset0:4 offset1:5
	ds_write2st64_b32 v2, v14, v1 offset0:6 offset1:7
	ds_write2st64_b32 v2, v12, v13 offset0:8 offset1:9
	ds_write2st64_b32 v2, v16, v8 offset0:10 offset1:11
	ds_write2st64_b32 v2, v9, v7 offset0:12 offset1:13
	ds_write2st64_b32 v2, v11, v0 offset0:14 offset1:15
	s_mov_b64 s[6:7], 0
	s_mov_b32 s8, 1
	s_cbranch_vccz .LBB0_704
	ds_read2st64_b32 v[0:1], v207 offset1:1
	ds_read2st64_b32 v[2:3], v207 offset0:2 offset1:3
	ds_read2st64_b32 v[4:5], v207 offset0:4 offset1:5
	ds_read2st64_b32 v[6:7], v207 offset0:6 offset1:7
	ds_read2st64_b32 v[16:17], v207 offset0:16 offset1:17
	ds_read2st64_b32 v[18:19], v207 offset0:18 offset1:19
	ds_read2st64_b32 v[20:21], v207 offset0:20 offset1:21
	ds_read2st64_b32 v[22:23], v207 offset0:22 offset1:23
	ds_read2st64_b32 v[8:9], v207 offset0:8 offset1:9
	ds_read2st64_b32 v[10:11], v207 offset0:10 offset1:11
	ds_read2st64_b32 v[12:13], v207 offset0:12 offset1:13
	ds_read2st64_b32 v[14:15], v207 offset0:14 offset1:15
	ds_read2st64_b32 v[24:25], v207 offset0:24 offset1:25
	ds_read2st64_b32 v[26:27], v207 offset0:26 offset1:27
	ds_read2st64_b32 v[28:29], v207 offset0:28 offset1:29
	ds_read2st64_b32 v[30:31], v207 offset0:30 offset1:31
	s_and_saveexec_b64 s[8:9], s[38:39]
	s_cbranch_execz .LBB0_696
	s_waitcnt lgkmcnt(0)
	v_and_b32_e32 v49, 0xffffff80, v30
	v_and_b32_e32 v48, 0xffffff80, v0
	v_and_b32_e32 v39, 0xffffff80, v19
	v_and_b32_e32 v38, 0xffffff80, v20
	v_pk_add_f32 v[52:53], v[38:39], v[48:49] op_sel:[1,0] op_sel_hi:[0,1]
	v_cmp_gt_i32_e32 vcc, 0, v52
	v_bfrev_b32_e32 v43, 0.5
	s_movk_i32 s12, 0xff00
	v_cndmask_b32_e64 v43, v43, 3, vcc
	v_and_b32_e32 v42, 0xffffff80, v23
	v_and_or_b32 v56, v52, s12, v43
	v_mov_b32_e32 v43, v38
	v_pk_add_f32 v[52:53], v[48:49], v[42:43] op_sel_hi:[0,1]
	v_cmp_gt_i32_e32 vcc, 0, v53
	v_mov_b32_e32 v54, 0xfb
	v_and_b32_e32 v41, 0xffffff80, v22
	v_cndmask_b32_e64 v54, v54, 4, vcc
	v_and_b32_e32 v40, 0xffffff80, v21
	v_and_or_b32 v53, v53, s12, v54
	v_cmp_gt_i32_e32 vcc, 0, v52
	v_mov_b32_e32 v54, 0xf8
	v_mov_b32_e32 v58, 0xf9
	v_cndmask_b32_e64 v57, v54, 7, vcc
	v_pk_add_f32 v[54:55], v[48:49], v[40:41] op_sel_hi:[0,1]
	v_cmp_gt_i32_e32 vcc, 0, v55
	v_mov_b32_e32 v59, 0xfa
	v_and_b32_e32 v55, 0xffffff00, v55
	v_cndmask_b32_e64 v58, v58, 6, vcc
	v_cmp_gt_i32_e32 vcc, 0, v54
	v_and_b32_e32 v54, 0xffffff00, v54
	v_and_b32_e32 v52, 0xffffff00, v52
	v_cndmask_b32_e64 v59, v59, 5, vcc
	v_or_b32_e32 v55, v58, v55
	v_or_b32_e32 v54, v59, v54
	v_or_b32_e32 v52, v57, v52
	v_writelane_b32 v255, s8, 44
	v_min_f32_e32 v57, v55, v52
	v_max_f32_e32 v58, v53, v54
	v_min_f32_e32 v53, v53, v54
	v_max_f32_e32 v52, v55, v52
	v_writelane_b32 v255, s9, 45
	v_and_b32_e32 v45, 0xffffff80, v24
	v_and_b32_e32 v44, 0xffffff80, v27
	v_min_f32_e32 v59, v58, v57
	v_min_f32_e32 v54, v53, v52
	v_max_f32_e32 v57, v58, v57
	v_max_f32_e32 v52, v53, v52
	v_pk_add_f32 v[44:45], v[48:49], v[44:45] op_sel_hi:[0,1]
	v_and_b32_e32 v47, 0xffffff80, v26
	v_min_f32_e32 v58, v57, v52
	v_max_f32_e32 v57, v57, v52
	v_cmp_gt_i32_e32 vcc, 0, v45
	v_mov_b32_e32 v52, 0xf7
	v_and_b32_e32 v46, 0xffffff80, v25
	v_cndmask_b32_e64 v52, v52, 8, vcc
	v_and_or_b32 v45, v45, s12, v52
	v_cmp_gt_i32_e32 vcc, 0, v44
	v_mov_b32_e32 v52, 0xf4
	v_pk_add_f32 v[46:47], v[48:49], v[46:47] op_sel_hi:[0,1]
	v_cndmask_b32_e64 v52, v52, 11, vcc
	v_cmp_gt_i32_e32 vcc, 0, v47
	v_mov_b32_e32 v53, 0xf5
	v_min_f32_e32 v55, v59, v54
	v_max_f32_e32 v59, v59, v54
	v_cndmask_b32_e64 v53, v53, 10, vcc
	v_cmp_gt_i32_e32 vcc, 0, v46
	v_mov_b32_e32 v54, 0xf6
	v_and_b32_e32 v47, 0xffffff00, v47
	v_cndmask_b32_e64 v54, v54, 9, vcc
	v_and_b32_e32 v46, 0xffffff00, v46
	v_and_b32_e32 v44, 0xffffff00, v44
	v_or_b32_e32 v47, v53, v47
	v_or_b32_e32 v46, v54, v46
	v_or_b32_e32 v44, v52, v44
	v_and_b32_e32 v51, 0xffffff80, v29
	v_and_b32_e32 v50, 0xffffff80, v28
	v_writelane_b32 v255, s11, 46
	v_min_f32_e32 v52, v47, v44
	v_max_f32_e32 v53, v45, v46
	v_min_f32_e32 v46, v45, v46
	v_max_f32_e32 v47, v47, v44
	v_pk_add_f32 v[44:45], v[48:49], v[50:51] op_sel_hi:[0,1]
	v_cmp_gt_i32_e64 s[10:11], 0, v45
	v_mov_b32_e32 v50, 0xf2
	v_mov_b32_e32 v51, 0xf3
	v_cndmask_b32_e64 v50, v50, 13, s[10:11]
	v_cmp_gt_i32_e64 s[10:11], 0, v44
	v_and_b32_e32 v45, 0xffffff00, v45
	v_and_b32_e32 v44, 0xffffff00, v44
	v_cndmask_b32_e64 v51, v51, 12, s[10:11]
	v_or_b32_e32 v50, v50, v45
	v_or_b32_e32 v51, v51, v44
	v_and_b32_e32 v45, 0xffffff80, v31
	v_mov_b32_e32 v44, v49
	v_pk_add_f32 v[44:45], v[48:49], v[44:45] op_sel_hi:[0,1]
	v_cmp_gt_i32_e64 s[42:43], 0, v45
	v_mov_b32_e32 v249, 0xf0
	v_mov_b32_e32 v173, 0xf1
	v_cndmask_b32_e64 v63, v249, 15, s[42:43]
	v_cmp_gt_i32_e64 s[42:43], 0, v44
	v_and_b32_e32 v45, 0xffffff00, v45
	v_and_b32_e32 v44, 0xffffff00, v44
	v_cndmask_b32_e64 v173, v173, 14, s[42:43]
	v_or_b32_e32 v45, v63, v45
	v_or_b32_e32 v44, v173, v44
	v_max_f32_e32 v62, v51, v50
	v_min_f32_e32 v63, v44, v45
	v_min_f32_e32 v50, v51, v50
	v_max_f32_e32 v44, v44, v45
	v_max_f32_e32 v54, v53, v52
	v_max_f32_e32 v60, v46, v47
	v_min_f32_e32 v173, v62, v63
	v_min_f32_e32 v45, v50, v44
	v_min_f32_e32 v51, v53, v52
	v_min_f32_e32 v46, v46, v47
	v_max_f32_e32 v52, v62, v63
	v_max_f32_e32 v44, v50, v44
	v_max_f32_e32 v61, v54, v60
	v_min_f32_e32 v178, v173, v45
	v_max_f32_e32 v47, v51, v46
	v_min_f32_e32 v50, v52, v44
	v_min_f32_e32 v54, v54, v60
	v_max_f32_e32 v45, v173, v45
	v_min_f32_e32 v46, v51, v46
	v_max_f32_e32 v44, v52, v44
	v_min_f32_e32 v179, v61, v178
	v_min_f32_e32 v53, v47, v50
	v_min_f32_e32 v60, v54, v45
	v_min_f32_e32 v52, v46, v44
	v_max_f32_e32 v61, v61, v178
	v_max_f32_e32 v47, v47, v50
	v_max_f32_e32 v45, v54, v45
	v_max_f32_e32 v44, v46, v44
	v_min_f32_e32 v62, v179, v53
	v_min_f32_e32 v63, v60, v52
	v_min_f32_e32 v50, v61, v47
	v_min_f32_e32 v46, v45, v44
	v_max_f32_e32 v53, v179, v53
	v_max_f32_e32 v52, v60, v52
	v_max_f32_e32 v47, v61, v47
	v_max_f32_e32 v44, v45, v44
	v_min_f32_e32 v60, v53, v52
	v_min_f32_e32 v61, v47, v44
	v_max_f32_e32 v52, v53, v52
	v_max_f32_e32 v53, v47, v44
	v_and_b32_e32 v44, 0xffffff80, v1
	v_add_f32_e32 v45, v39, v44
	v_min_f32_e32 v51, v62, v63
	v_min_f32_e32 v173, v50, v46
	v_max_f32_e32 v62, v62, v63
	v_max_f32_e32 v63, v50, v46
	v_cmp_gt_i32_e32 vcc, 0, v45
	v_mov_b32_e32 v46, 0xec
	v_mov_b32_e32 v47, 0xe9
	v_cndmask_b32_e64 v46, v46, 19, vcc
	v_and_or_b32 v45, v45, s12, v46
	v_pk_add_f32 v[42:43], v[44:45], v[42:43] op_sel_hi:[0,1]
	v_cmp_gt_i32_e32 vcc, 0, v43
	v_mov_b32_e32 v46, 0xeb
	v_pk_add_f32 v[40:41], v[44:45], v[40:41] op_sel_hi:[0,1]
	v_cndmask_b32_e64 v46, v46, 20, vcc
	v_and_or_b32 v43, v43, s12, v46
	v_cmp_gt_i32_e32 vcc, 0, v42
	v_mov_b32_e32 v46, 0xe8
	v_mov_b32_e32 v50, 0xea
	v_cndmask_b32_e64 v46, v46, 23, vcc
	v_cmp_gt_i32_e32 vcc, 0, v41
	v_and_b32_e32 v41, 0xffffff00, v41
	v_and_b32_e32 v42, 0xffffff00, v42
	v_cndmask_b32_e64 v47, v47, 22, vcc
	v_cmp_gt_i32_e32 vcc, 0, v40
	v_and_b32_e32 v40, 0xffffff00, v40
	v_or_b32_e32 v41, v47, v41
	v_cndmask_b32_e64 v50, v50, 21, vcc
	v_or_b32_e32 v40, v50, v40
	v_or_b32_e32 v42, v46, v42
	v_and_b32_e32 v182, 0xffffff80, v3
	v_min_f32_e32 v46, v41, v42
	v_max_f32_e32 v47, v43, v40
	v_min_f32_e32 v40, v43, v40
	v_max_f32_e32 v41, v41, v42
	v_and_b32_e32 v37, 0xffffff80, v4
	v_max_f32_e32 v43, v47, v46
	v_min_f32_e32 v42, v40, v41
	v_max_f32_e32 v40, v40, v41
	v_min_f32_e32 v50, v47, v46
	v_and_b32_e32 v46, 0xffffff80, v2
	v_and_b32_e32 v36, 0xffffff80, v18
	v_min_f32_e32 v179, v43, v40
	v_max_f32_e32 v180, v43, v40
	v_pk_add_f32 v[40:41], v[46:47], v[38:39] op_sel_hi:[0,1]
	v_cmp_gt_i32_e32 vcc, 0, v41
	v_mov_b32_e32 v38, 0xdc
	v_and_b32_e32 v35, 0xffffff80, v7
	v_cndmask_b32_e64 v38, v38, 35, vcc
	v_and_or_b32 v41, v41, s12, v38
	v_cmp_gt_i32_e32 vcc, 0, v40
	v_mov_b32_e32 v38, 0xdb
	v_and_b32_e32 v34, 0xffffff80, v17
	v_cndmask_b32_e64 v38, v38, 36, vcc
	v_and_or_b32 v181, v40, s12, v38
	v_add_f32_e32 v38, v39, v182
	v_cmp_gt_i32_e32 vcc, 0, v38
	v_mov_b32_e32 v39, 0xcc
	s_nop 0
	v_cndmask_b32_e64 v39, v39, 51, vcc
	v_and_or_b32 v54, v38, s12, v39
	v_pk_add_f32 v[38:39], v[48:49], v[36:37]
	v_min_f32_e32 v178, v50, v42
	v_cmp_gt_i32_e32 vcc, 0, v38
	v_bfrev_b32_e32 v39, -0.5
	v_max_f32_e32 v50, v50, v42
	v_cndmask_b32_e64 v39, v39, 2, vcc
	v_and_or_b32 v38, v38, s12, v39
	v_mov_b32_e32 v39, 0xed
	v_and_b32_e32 v43, 0xffffff80, v6
	v_min_f32_e32 v183, v38, v56
	v_max_f32_e32 v56, v38, v56
	v_add_f32_e32 v38, v36, v44
	v_cmp_gt_i32_e32 vcc, 0, v38
	v_and_b32_e32 v42, 0xffffff80, v5
	v_and_b32_e32 v33, 0xffffff80, v14
	v_cndmask_b32_e64 v39, v39, 18, vcc
	v_and_or_b32 v38, v38, s12, v39
	v_mov_b32_e32 v39, 0xdd
	v_and_b32_e32 v32, 0xffffff80, v16
	v_min_f32_e32 v190, v38, v45
	v_max_f32_e32 v195, v38, v45
	v_add_f32_e32 v38, v36, v46
	v_cmp_gt_i32_e32 vcc, 0, v38
	v_mov_b32_e32 v45, 0x61
	v_mov_b32_e32 v234, 0xef
	v_cndmask_b32_e64 v39, v39, 34, vcc
	v_and_or_b32 v38, v38, s12, v39
	v_mov_b32_e32 v39, 0xcd
	v_mov_b32_e32 v241, 0xdf
	v_min_f32_e32 v209, v38, v41
	v_max_f32_e32 v210, v38, v41
	v_add_f32_e32 v38, v36, v182
	v_cmp_gt_i32_e32 vcc, 0, v38
	v_mov_b32_e32 v41, 0x42
	v_mov_b32_e32 v244, 0xcf
	v_cndmask_b32_e64 v39, v39, 50, vcc
	v_and_or_b32 v40, v38, s12, v39
	v_pk_add_f32 v[38:39], v[36:37], v[36:37] op_sel:[1,0] op_sel_hi:[0,1]
	v_cmp_gt_i32_e32 vcc, 0, v38
	v_mov_b32_e32 v39, 0xbd
	v_and_b32_e32 v47, 0xffffff80, v8
	v_cndmask_b32_e32 v39, v39, v41, vcc
	v_and_or_b32 v41, v38, s12, v39
	v_pk_add_f32 v[38:39], v[48:49], v[34:35]
	v_pk_add_f32 v[48:49], v[48:49], v[32:33]
	v_cmp_gt_i32_e32 vcc, 0, v38
	v_mov_b32_e32 v39, 0xfe
	s_mov_b32 s28, 0xff61b1e6
	v_cndmask_b32_e64 v39, v39, 1, vcc
	v_and_or_b32 v211, v38, s12, v39
	v_add_f32_e32 v38, v34, v44
	v_cmp_gt_i32_e32 vcc, 0, v38
	v_mov_b32_e32 v39, 0xee
	v_add_f32_e32 v44, v32, v44
	v_cndmask_b32_e64 v39, v39, 17, vcc
	v_and_or_b32 v212, v38, s12, v39
	v_add_f32_e32 v38, v34, v46
	v_cmp_gt_i32_e32 vcc, 0, v38
	v_mov_b32_e32 v39, 0xde
	v_add_f32_e32 v46, v32, v46
	v_cndmask_b32_e64 v39, v39, 33, vcc
	v_and_or_b32 v213, v38, s12, v39
	v_add_f32_e32 v38, v34, v182
	v_cmp_gt_i32_e32 vcc, 0, v38
	v_mov_b32_e32 v39, 0xce
	v_add_f32_e32 v182, v32, v182
	v_cndmask_b32_e64 v39, v39, 49, vcc
	v_and_or_b32 v38, v38, s12, v39
	v_cmp_gt_i32_e64 s[74:75], 0, v46
	v_cmp_gt_i32_e64 s[84:85], 0, v182
	v_min_f32_e32 v219, v38, v40
	v_max_f32_e32 v220, v38, v40
	v_pk_add_f32 v[38:39], v[36:37], v[34:35] op_sel:[1,0] op_sel_hi:[0,1]
	v_cmp_gt_i32_e32 vcc, 0, v38
	v_mov_b32_e32 v39, 0xbe
	v_mov_b32_e32 v40, 0x41
	v_cndmask_b32_e32 v39, v39, v40, vcc
	v_and_or_b32 v38, v38, s12, v39
	v_mov_b32_e32 v40, v35
	v_cndmask_b32_e64 v241, v241, 32, s[74:75]
	v_min_f32_e32 v215, v38, v41
	v_max_f32_e32 v216, v38, v41
	v_pk_add_f32 v[38:39], v[34:35], v[42:43]
	v_mov_b32_e32 v41, v43
	v_pk_add_f32 v[40:41], v[34:35], v[40:41] op_sel_hi:[0,1]
	v_cmp_gt_i32_e32 vcc, 0, v38
	v_mov_b32_e32 v34, 0xae
	v_mov_b32_e32 v39, 0x51
	v_cndmask_b32_e32 v34, v34, v39, vcc
	v_cmp_gt_i32_e32 vcc, 0, v41
	v_mov_b32_e32 v39, 0x9e
	v_and_b32_e32 v38, 0xffffff00, v38
	v_cndmask_b32_e32 v39, v39, v45, vcc
	v_or_b32_e32 v218, v34, v38
	v_cmp_gt_i32_e32 vcc, 0, v40
	v_mov_b32_e32 v34, 0x8e
	v_mov_b32_e32 v38, 0x71
	v_cndmask_b32_e32 v34, v34, v38, vcc
	v_and_or_b32 v214, v40, s12, v34
	v_cmp_gt_i32_e32 vcc, 0, v48
	v_mov_b32_e32 v34, 0xff
	v_cndmask_b32_e64 v244, v244, 48, s[84:85]
	v_cndmask_b32_e64 v34, v34, 0, vcc
	v_and_or_b32 v34, v48, s12, v34
	v_and_or_b32 v46, v46, s12, v241
	v_and_or_b32 v182, v182, s12, v244
	v_max_f32_e32 v48, v34, v211
	v_min_f32_e32 v34, v34, v211
	v_max_f32_e32 v49, v48, v183
	v_max_f32_e32 v211, v34, v56
	v_min_f32_e32 v48, v48, v183
	v_min_f32_e32 v34, v34, v56
	v_max_f32_e32 v221, v49, v211
	v_max_f32_e32 v56, v48, v34
	v_min_f32_e32 v49, v49, v211
	v_min_f32_e32 v34, v48, v34
	v_max_f32_e32 v222, v221, v55
	v_max_f32_e32 v183, v56, v58
	v_max_f32_e32 v211, v49, v59
	v_max_f32_e32 v48, v34, v57
	v_min_f32_e32 v55, v221, v55
	v_min_f32_e32 v56, v56, v58
	v_min_f32_e32 v49, v49, v59
	v_min_f32_e32 v34, v34, v57
	v_max_f32_e32 v241, v46, v213
	v_max_f32_e32 v58, v55, v56
	v_max_f32_e32 v57, v49, v34
	v_min_f32_e32 v55, v55, v56
	v_min_f32_e32 v34, v49, v34
	v_min_f32_e32 v46, v46, v213
	v_max_f32_e32 v244, v181, v182
	v_max_f32_e32 v49, v55, v34
	v_min_f32_e32 v34, v55, v34
	v_cmp_gt_i32_e64 s[6:7], 0, v44
	v_min_f32_e32 v181, v181, v182
	s_nop 0
	v_cndmask_b32_e64 v234, v234, 16, s[6:7]
	v_and_or_b32 v44, v44, s12, v234
	v_max_f32_e32 v234, v44, v212
	v_min_f32_e32 v44, v44, v212
	v_max_f32_e32 v235, v234, v190
	v_max_f32_e32 v212, v44, v195
	v_min_f32_e32 v190, v234, v190
	v_min_f32_e32 v44, v44, v195
	v_max_f32_e32 v242, v241, v209
	v_max_f32_e32 v213, v46, v210
	v_min_f32_e32 v245, v244, v219
	v_min_f32_e32 v182, v181, v220
	v_min_f32_e32 v209, v241, v209
	v_min_f32_e32 v46, v46, v210
	v_max_f32_e32 v219, v244, v219
	v_max_f32_e32 v181, v181, v220
	v_max_f32_e32 v59, v58, v57
	v_min_f32_e32 v57, v58, v57
	v_max_f32_e32 v236, v235, v212
	v_max_f32_e32 v195, v190, v44
	v_min_f32_e32 v212, v235, v212
	v_min_f32_e32 v44, v190, v44
	v_max_f32_e32 v243, v242, v213
	v_min_f32_e32 v246, v245, v182
	v_max_f32_e32 v210, v209, v46
	v_min_f32_e32 v220, v219, v181
	v_min_f32_e32 v213, v242, v213
	v_max_f32_e32 v182, v245, v182
	v_min_f32_e32 v46, v209, v46
	v_max_f32_e32 v181, v219, v181
	v_max_f32_e32 v237, v236, v178
	v_max_f32_e32 v234, v195, v179
	v_max_f32_e32 v235, v212, v50
	v_max_f32_e32 v190, v44, v180
	v_min_f32_e32 v247, v243, v246
	v_min_f32_e32 v241, v210, v220
	v_min_f32_e32 v242, v213, v182
	v_min_f32_e32 v209, v46, v181
	v_min_f32_e32 v178, v236, v178
	v_min_f32_e32 v179, v195, v179
	v_min_f32_e32 v50, v212, v50
	v_min_f32_e32 v44, v44, v180
	v_max_f32_e32 v236, v243, v246
	v_max_f32_e32 v210, v210, v220
	v_max_f32_e32 v182, v213, v182
	v_max_f32_e32 v46, v46, v181
	v_max_f32_e32 v223, v222, v183
	v_max_f32_e32 v224, v211, v48
	v_min_f32_e32 v183, v222, v183
	v_min_f32_e32 v48, v211, v48
	v_max_f32_e32 v238, v237, v234
	v_max_f32_e32 v239, v235, v190
	v_min_f32_e32 v244, v247, v241
	v_min_f32_e32 v219, v242, v209
	v_max_f32_e32 v195, v178, v179
	v_max_f32_e32 v180, v50, v44
	v_min_f32_e32 v220, v236, v210
	v_min_f32_e32 v181, v182, v46
	v_min_f32_e32 v234, v237, v234
	v_min_f32_e32 v190, v235, v190
	v_max_f32_e32 v237, v247, v241
	v_max_f32_e32 v209, v242, v209
	v_min_f32_e32 v178, v178, v179
	v_min_f32_e32 v44, v50, v44
	v_max_f32_e32 v50, v236, v210
	v_max_f32_e32 v46, v182, v46
	v_max_f32_e32 v225, v223, v224
	v_max_f32_e32 v211, v183, v48
	v_min_f32_e32 v223, v223, v224
	v_min_f32_e32 v48, v183, v48
	v_max_f32_e32 v240, v238, v239
	v_min_f32_e32 v245, v244, v219
	v_max_f32_e32 v212, v195, v180
	v_min_f32_e32 v213, v220, v181
	v_max_f32_e32 v235, v234, v190
	v_min_f32_e32 v241, v237, v209
	v_max_f32_e32 v179, v178, v44
	v_min_f32_e32 v182, v50, v46
	v_min_f32_e32 v238, v238, v239
	v_max_f32_e32 v219, v244, v219
	v_min_f32_e32 v180, v195, v180
	v_max_f32_e32 v181, v220, v181
	v_min_f32_e32 v190, v234, v190
	v_max_f32_e32 v209, v237, v209
	v_min_f32_e32 v44, v178, v44
	v_max_f32_e32 v46, v50, v46
	v_max_f32_e32 v226, v225, v51
	v_max_f32_e32 v221, v59, v173
	v_max_f32_e32 v222, v211, v60
	v_max_f32_e32 v56, v49, v61
	v_max_f32_e32 v224, v223, v62
	v_max_f32_e32 v58, v57, v63
	v_max_f32_e32 v183, v48, v52
	v_max_f32_e32 v55, v34, v53
	v_min_f32_e32 v248, v240, v245
	v_min_f32_e32 v243, v212, v213
	v_min_f32_e32 v242, v235, v241
	v_min_f32_e32 v210, v179, v182
	v_min_f32_e32 v239, v238, v219
	v_min_f32_e32 v195, v180, v181
	v_min_f32_e32 v234, v190, v209
	v_min_f32_e32 v178, v44, v46
	v_max_f32_e32 v227, v226, v221
	v_max_f32_e32 v228, v222, v56
	v_max_f32_e32 v230, v224, v58
	v_max_f32_e32 v231, v183, v55
	v_min_f32_e32 v246, v248, v243
	v_min_f32_e32 v236, v242, v210
	v_min_f32_e32 v220, v239, v195
	v_min_f32_e32 v237, v234, v178
	v_max_f32_e32 v229, v227, v228
	v_max_f32_e32 v232, v230, v231
	v_min_f32_e32 v247, v246, v236
	v_min_f32_e32 v244, v220, v237
	v_min_f32_e32 v51, v225, v51
	v_min_f32_e32 v59, v59, v173
	v_min_f32_e32 v60, v211, v60
	v_min_f32_e32 v61, v49, v61
	v_min_f32_e32 v62, v223, v62
	v_min_f32_e32 v57, v57, v63
	v_min_f32_e32 v48, v48, v52
	v_min_f32_e32 v34, v34, v53
	v_max_f32_e32 v63, v240, v245
	v_max_f32_e32 v212, v212, v213
	v_max_f32_e32 v235, v235, v241
	v_max_f32_e32 v179, v179, v182
	v_max_f32_e32 v219, v238, v219
	v_max_f32_e32 v180, v180, v181
	v_max_f32_e32 v190, v190, v209
	v_max_f32_e32 v44, v44, v46
	v_max_f32_e32 v233, v229, v232
	v_min_f32_e32 v50, v247, v244
	v_max_f32_e32 v173, v51, v59
	v_max_f32_e32 v211, v60, v61
	v_max_f32_e32 v223, v62, v57
	v_max_f32_e32 v53, v48, v34
	v_min_f32_e32 v213, v63, v212
	v_min_f32_e32 v182, v235, v179
	v_min_f32_e32 v181, v219, v180
	v_min_f32_e32 v46, v190, v44
	v_min_f32_e32 v227, v227, v228
	v_min_f32_e32 v228, v230, v231
	v_max_f32_e32 v230, v246, v236
	v_max_f32_e32 v220, v220, v237
	v_max_f32_e32 v50, v233, v50
	v_max_f32_e32 v44, v190, v44
	v_max_f32_e32 v225, v173, v211
	v_max_f32_e32 v233, v223, v53
	v_min_f32_e32 v240, v213, v182
	v_min_f32_e32 v209, v181, v46
	v_min_f32_e32 v221, v226, v221
	v_min_f32_e32 v222, v222, v56
	v_min_f32_e32 v224, v224, v58
	v_min_f32_e32 v183, v183, v55
	v_max_f32_e32 v241, v248, v243
	v_max_f32_e32 v210, v242, v210
	v_max_f32_e32 v195, v239, v195
	v_max_f32_e32 v234, v234, v178
	v_min_f32_e32 v51, v51, v59
	v_min_f32_e32 v59, v60, v61
	v_min_f32_e32 v57, v62, v57
	v_min_f32_e32 v34, v48, v34
	v_max_f32_e32 v60, v63, v212
	v_max_f32_e32 v62, v235, v179
	v_max_f32_e32 v58, v227, v228
	v_min_f32_e32 v63, v230, v220
	v_min_f32_e32 v211, v173, v211
	v_min_f32_e32 v223, v223, v53
	v_max_f32_e32 v213, v213, v182
	v_max_f32_e32 v46, v181, v46
	v_max_f32_e32 v226, v221, v222
	v_max_f32_e32 v238, v224, v183
	v_max_f32_e32 v243, v51, v59
	v_max_f32_e32 v245, v57, v34
	v_min_f32_e32 v179, v60, v62
	v_max_f32_e32 v63, v58, v63
	v_max_f32_e32 v53, v211, v223
	v_min_f32_e32 v58, v213, v46
	v_min_f32_e32 v181, v221, v222
	v_min_f32_e32 v221, v224, v183
	v_max_f32_e32 v222, v241, v210
	v_max_f32_e32 v224, v195, v234
	v_min_f32_e32 v51, v51, v59
	v_min_f32_e32 v59, v57, v34
	v_max_f32_e32 v231, v60, v62
	v_min_f32_e32 v57, v229, v232
	v_max_f32_e32 v62, v247, v244
	v_min_f32_e32 v239, v195, v234
	v_min_f32_e32 v242, v241, v210
	v_max_f32_e32 v212, v219, v180
	v_max_f32_e32 v178, v53, v58
	v_max_f32_e32 v53, v181, v221
	v_min_f32_e32 v173, v222, v224
	v_max_f32_e32 v183, v57, v62
	v_min_f32_e32 v57, v225, v233
	v_max_f32_e32 v62, v240, v209
	v_min_f32_e32 v219, v212, v44
	v_max_f32_e32 v180, v53, v173
	v_max_f32_e32 v190, v57, v62
	v_min_f32_e32 v57, v226, v238
	v_max_f32_e32 v173, v242, v239
	v_max_f32_e32 v55, v226, v238
	v_min_f32_e32 v56, v242, v239
	v_max_f32_e32 v210, v230, v220
	v_max_f32_e32 v195, v57, v173
	v_min_f32_e32 v57, v243, v245
	v_max_f32_e32 v173, v179, v219
	v_max_f32_e32 v55, v55, v56
	v_min_f32_e32 v56, v179, v219
	v_min_f32_e32 v179, v227, v228
	v_min_f32_e32 v52, v240, v209
	v_max_f32_e32 v209, v57, v173
	v_max_f32_e32 v46, v213, v46
	v_max_f32_e32 v44, v212, v44
	v_max_f32_e32 v210, v179, v210
	v_min_f32_e32 v179, v211, v223
	v_max_f32_e32 v211, v179, v46
	v_min_f32_e32 v46, v181, v221
	v_max_f32_e32 v181, v222, v224
	v_min_f32_e32 v53, v231, v44
	v_max_f32_e32 v44, v231, v44
	v_max_f32_e32 v212, v46, v181
	v_min_f32_e32 v46, v51, v59
	v_max_f32_e32 v34, v51, v59
	v_pk_add_f32 v[36:37], v[36:37], v[32:33] op_sel:[1,0] op_sel_hi:[0,1]
	v_mov_b32_e32 v37, 0xbf
	v_max_f32_e32 v213, v46, v44
	v_cmp_gt_i32_e32 vcc, 0, v36
	v_mov_b32_e32 v221, 0x50
	v_and_b32_e32 v41, 0xffffff00, v41
	v_cndmask_b32_e64 v37, v37, 64, vcc
	v_and_or_b32 v36, v36, s12, v37
	v_or_b32_e32 v217, v39, v41
	v_max_f32_e32 v49, v225, v233
	v_max_f32_e32 v44, v54, v36
	v_min_f32_e32 v54, v54, v36
	v_pk_add_f32 v[36:37], v[32:33], v[42:43] op_sel_hi:[0,1]
	v_cmp_gt_i32_e64 s[68:69], 0, v37
	v_mov_b32_e32 v42, 0x9f
	v_mov_b32_e32 v43, 0x60
	v_cndmask_b32_e64 v42, v42, v43, s[68:69]
	v_cmp_gt_i32_e64 s[68:69], 0, v36
	v_mov_b32_e32 v43, 0xaf
	v_and_b32_e32 v37, 0xffffff00, v37
	v_cndmask_b32_e64 v43, v43, v221, s[68:69]
	v_and_b32_e32 v36, 0xffffff00, v36
	v_or_b32_e32 v37, v42, v37
	v_or_b32_e32 v36, v43, v36
	v_min_f32_e32 v42, v37, v217
	v_max_f32_e32 v43, v36, v218
	v_max_f32_e32 v37, v37, v217
	v_min_f32_e32 v36, v36, v218
	v_max_f32_e32 v46, v44, v215
	v_max_f32_e32 v219, v54, v216
	v_min_f32_e32 v221, v43, v42
	v_min_f32_e32 v217, v36, v37
	v_max_f32_e32 v42, v43, v42
	v_max_f32_e32 v36, v36, v37
	v_max_f32_e32 v220, v46, v219
	v_min_f32_e32 v44, v44, v215
	v_min_f32_e32 v54, v54, v216
	v_min_f32_e32 v219, v46, v219
	v_mov_b32_e32 v46, v35
	v_min_f32_e32 v216, v42, v36
	v_max_f32_e32 v225, v42, v36
	v_pk_add_f32 v[36:37], v[32:33], v[46:47] op_sel_hi:[0,1]
	v_and_b32_e32 v45, 0xffffff80, v9
	v_max_f32_e32 v215, v44, v54
	v_min_f32_e32 v54, v44, v54
	v_mov_b32_e32 v44, v35
	v_cmp_gt_i32_e32 vcc, 0, v37
	v_mov_b32_e32 v35, 0x7f
	v_pk_add_f32 v[42:43], v[32:33], v[44:45] op_sel_hi:[0,1]
	v_cndmask_b32_e32 v35, v35, v196, vcc
	v_cmp_gt_i32_e32 vcc, 0, v36
	v_mov_b32_e32 v47, 0x8f
	v_mov_b32_e32 v45, 0x6f
	v_cndmask_b32_e32 v44, v47, v198, vcc
	v_cmp_gt_i32_e32 vcc, 0, v43
	v_mov_b32_e32 v46, 0x90
	v_and_b32_e32 v37, 0xffffff00, v37
	v_and_b32_e32 v36, 0xffffff00, v36
	v_cndmask_b32_e32 v45, v45, v46, vcc
	v_and_b32_e32 v43, 0xffffff00, v43
	v_cmp_gt_i32_e32 vcc, 0, v42
	v_or_b32_e32 v35, v35, v37
	v_or_b32_e32 v36, v44, v36
	v_or_b32_e32 v37, v45, v43
	v_and_b32_e32 v41, 0xffffff80, v10
	v_and_b32_e32 v40, 0xffffff80, v13
	v_cndmask_b32_e32 v46, v47, v198, vcc
	v_cmp_lt_f32_e32 vcc, v37, v35
	v_cmp_lt_f32_e64 s[8:9], v214, v36
	v_and_b32_e32 v39, 0xffffff80, v12
	v_cndmask_b32_e32 v43, v35, v37, vcc
	v_cndmask_b32_e64 v45, v36, v214, s[8:9]
	v_cndmask_b32_e32 v35, v37, v35, vcc
	v_pk_add_f32 v[36:37], v[32:33], v[40:41] op_sel_hi:[0,1]
	v_cmp_gt_i32_e64 s[80:81], 0, v37
	v_mov_b32_e32 v40, 0x5f
	v_mov_b32_e32 v41, 0xa0
	v_and_b32_e32 v38, 0xffffff80, v11
	v_cndmask_b32_e64 v40, v40, v41, s[80:81]
	v_and_b32_e32 v42, 0xffffff00, v42
	v_and_or_b32 v37, v37, s12, v40
	v_cmp_gt_i32_e64 s[80:81], 0, v36
	v_mov_b32_e32 v40, 0xd0
	v_pk_add_f32 v[38:39], v[32:33], v[38:39] op_sel_hi:[0,1]
	v_or_b32_e32 v42, v46, v42
	v_cndmask_b32_e64 v40, 47, v40, s[80:81]
	v_cmp_gt_i32_e64 s[80:81], 0, v39
	v_mov_b32_e32 v41, 0xc0
	v_cndmask_b32_e64 v42, v214, v42, s[8:9]
	v_cndmask_b32_e64 v41, 63, v41, s[80:81]
	v_cmp_gt_i32_e64 s[80:81], 0, v38
	v_mov_b32_e32 v214, 0x4f
	v_mov_b32_e32 v229, 0xb0
	v_cndmask_b32_e64 v214, v214, v229, s[80:81]
	v_and_b32_e32 v39, 0xffffff00, v39
	v_and_b32_e32 v38, 0xffffff00, v38
	v_and_b32_e32 v36, 0xffffff00, v36
	v_or_b32_e32 v39, v41, v39
	v_or_b32_e32 v38, v214, v38
	v_or_b32_e32 v36, v40, v36
	v_min_f32_e32 v40, v39, v36
	v_max_f32_e32 v41, v37, v38
	v_min_f32_e32 v37, v37, v38
	v_max_f32_e32 v36, v39, v36
	v_max_f32_e32 v44, v42, v43
	v_max_f32_e32 v46, v45, v35
	v_min_f32_e32 v214, v41, v40
	v_min_f32_e32 v38, v37, v36
	v_min_f32_e32 v42, v42, v43
	v_min_f32_e32 v35, v45, v35
	v_max_f32_e32 v40, v41, v40
	v_max_f32_e32 v36, v37, v36
	v_max_f32_e32 v47, v44, v46
	v_min_f32_e32 v39, v214, v38
	v_max_f32_e32 v43, v42, v35
	v_min_f32_e32 v37, v40, v36
	v_min_f32_e32 v44, v44, v46
	v_max_f32_e32 v38, v214, v38
	v_min_f32_e32 v35, v42, v35
	v_max_f32_e32 v36, v40, v36
	v_min_f32_e32 v218, v221, v217
	v_max_f32_e32 v217, v221, v217
	v_min_f32_e32 v229, v47, v39
	v_min_f32_e32 v41, v43, v37
	v_min_f32_e32 v46, v44, v38
	v_min_f32_e32 v40, v35, v36
	v_max_f32_e32 v39, v47, v39
	v_max_f32_e32 v37, v43, v37
	v_max_f32_e32 v38, v44, v38
	v_max_f32_e32 v35, v35, v36
	v_max_f32_e32 v222, v220, v218
	v_max_f32_e32 v223, v215, v216
	v_max_f32_e32 v221, v219, v217
	v_max_f32_e32 v226, v54, v225
	v_min_f32_e32 v218, v220, v218
	v_min_f32_e32 v215, v215, v216
	v_min_f32_e32 v217, v219, v217
	v_min_f32_e32 v54, v54, v225
	v_min_f32_e32 v43, v39, v37
	v_min_f32_e32 v36, v38, v35
	v_max_f32_e32 v37, v39, v37
	v_max_f32_e32 v35, v38, v35
	v_max_f32_e32 v216, v218, v215
	v_max_f32_e32 v219, v217, v54
	v_min_f32_e32 v44, v43, v36
	v_min_f32_e32 v215, v218, v215
	v_min_f32_e32 v54, v217, v54
	v_min_f32_e32 v38, v37, v35
	v_max_f32_e32 v43, v43, v36
	v_max_f32_e32 v35, v37, v35
	v_and_b32_e32 v37, 0xffffff80, v15
	v_mov_b32_e32 v36, v33
	v_pk_add_f32 v[32:33], v[32:33], v[36:37] op_sel_hi:[0,1]
	v_mov_b32_e32 v37, 0xe0
	v_max_f32_e32 v217, v215, v54
	v_min_f32_e32 v54, v215, v54
	v_cmp_gt_i32_e64 s[76:77], 0, v33
	v_and_b32_e32 v33, 0xffffff00, v33
	s_nop 0
	v_cndmask_b32_e64 v36, 15, v249, s[76:77]
	v_cmp_gt_i32_e64 s[76:77], 0, v32
	v_and_b32_e32 v32, 0xffffff00, v32
	v_or_b32_e32 v33, v36, v33
	v_cndmask_b32_e64 v37, 31, v37, s[76:77]
	v_or_b32_e32 v32, v37, v32
	v_max_f32_e32 v36, v32, v33
	v_min_f32_e32 v32, v32, v33
	v_max_f32_e32 v37, v36, v36
	v_max_f32_e32 v33, v32, v32
	v_max_f32_e32 v37, 0xff61b1e6, v37
	v_max_f32_e32 v33, 0xff61b1e6, v33
	v_max_f32_e32 v224, v222, v223
	v_max_f32_e32 v233, v37, v33
	v_min_f32_e32 v33, v37, v33
	v_max_f32_e32 v234, 0xff61b1e6, v233
	v_max_f32_e32 v37, 0xff61b1e6, v33
	v_cmp_nlt_f32_e32 vcc, s28, v33
	v_max_f32_e32 v227, v221, v226
	v_max_f32_e32 v235, v234, v37
	v_cmp_nlt_f32_e64 s[88:89], s28, v235
	v_cndmask_b32_e32 v33, v199, v33, vcc
	v_min_f32_e32 v45, v229, v41
	v_cndmask_b32_e64 v236, v199, v235, s[88:89]
	v_cmp_nlt_f32_e64 s[88:89], s28, v233
	v_min_f32_e32 v42, v46, v40
	v_min_f32_e32 v222, v222, v223
	v_cndmask_b32_e64 v233, v199, v233, s[88:89]
	v_cmp_nlt_f32_e64 s[88:89], s28, v36
	v_min_f32_e32 v221, v221, v226
	v_max_f32_e32 v41, v229, v41
	v_cndmask_b32_e64 v36, v199, v36, s[88:89]
	v_cmp_nlt_f32_e64 s[88:89], s28, v32
	v_max_f32_e32 v40, v46, v40
	s_nop 0
	v_cndmask_b32_e64 v32, v199, v32, s[88:89]
	v_max_f32_e32 v237, v36, v32
	v_min_f32_e32 v32, v36, v32
	v_max_f32_e32 v238, v233, v237
	v_max_f32_e32 v36, v33, v32
	v_max_f32_e32 v228, v224, v227
	v_min_f32_e32 v214, v45, v42
	v_max_f32_e32 v220, v216, v219
	v_max_f32_e32 v223, v222, v221
	v_min_f32_e32 v46, v41, v40
	v_min_f32_e32 v224, v224, v227
	v_max_f32_e32 v42, v45, v42
	v_min_f32_e32 v216, v216, v219
	v_min_f32_e32 v221, v222, v221
	v_max_f32_e32 v40, v41, v40
	v_max_f32_e32 v239, v238, v36
	v_min_f32_e32 v233, v233, v237
	v_min_f32_e32 v32, v33, v32
	v_min_f32_e32 v37, v234, v37
	v_min_f32_e32 v36, v238, v36
	v_max_f32_e32 v52, v49, v52
	s_mov_b64 s[6:7], s[96:97]
	v_cmp_nlt_f32_e64 s[88:89], s28, v239
	v_cmp_nlt_f32_e64 s[76:77], s28, v37
	v_cmp_nlt_f32_e64 s[14:15], s28, v36
	v_max_f32_e32 v230, v228, v214
	v_max_f32_e32 v47, v220, v44
	v_max_f32_e32 v226, v223, v46
	v_max_f32_e32 v39, v217, v38
	v_max_f32_e32 v45, v224, v42
	v_max_f32_e32 v219, v216, v43
	v_max_f32_e32 v41, v221, v40
	v_max_f32_e32 v215, v54, v35
	v_cndmask_b32_e64 v240, v199, v239, s[88:89]
	v_max_f32_e32 v33, v233, v32
	v_cndmask_b32_e64 v234, v199, v37, s[76:77]
	v_cndmask_b32_e64 v238, v199, v36, s[14:15]
	v_min_f32_e32 v32, v233, v32
	v_cmp_nlt_f32_e64 s[88:89], s28, v33
	v_cmp_nlt_f32_e32 vcc, s28, v32
	v_max_f32_e32 v48, v243, v245
	v_max_f32_e32 v225, v230, v47
	v_max_f32_e32 v218, v226, v39
	v_max_f32_e32 v227, v45, v219
	v_max_f32_e32 v222, v41, v215
	v_min_f32_e32 v241, v236, v240
	v_cndmask_b32_e64 v237, v199, v33, s[88:89]
	v_min_f32_e32 v243, v234, v238
	v_cndmask_b32_e32 v233, v199, v32, vcc
	v_max_f32_e32 v229, v225, v218
	v_max_f32_e32 v231, v227, v222
	v_min_f32_e32 v242, v241, v237
	v_min_f32_e32 v244, v243, v233
	v_min_f32_e32 v214, v228, v214
	v_max_f32_e32 v232, v229, v231
	v_min_f32_e32 v245, v242, v244
	v_max_f32_e32 v228, 0xff61b1e6, v235
	v_max_f32_e32 v235, v239, v239
	v_max_f32_e32 v36, v36, v36
	v_min_f32_e32 v44, v220, v44
	v_min_f32_e32 v46, v223, v46
	v_min_f32_e32 v38, v217, v38
	v_min_f32_e32 v42, v224, v42
	v_min_f32_e32 v43, v216, v43
	v_min_f32_e32 v40, v221, v40
	v_min_f32_e32 v35, v54, v35
	v_max_f32_e32 v235, 0xff61b1e6, v235
	v_max_f32_e32 v33, v33, v33
	v_max_f32_e32 v37, 0xff61b1e6, v37
	v_max_f32_e32 v36, 0xff61b1e6, v36
	v_max_f32_e32 v32, v32, v32
	v_max_f32_e32 v232, v232, v245
	s_mov_b32 s36, s18
	v_max_f32_e32 v33, 0xff61b1e6, v33
	v_max_f32_e32 v32, 0xff61b1e6, v32
	v_max_f32_e32 v220, v214, v44
	v_max_f32_e32 v217, v46, v38
	v_max_f32_e32 v216, v42, v43
	v_max_f32_e32 v54, v40, v35
	v_min_f32_e32 v239, v228, v235
	v_min_f32_e32 v245, 0xff61b1e6, v33
	v_min_f32_e32 v247, v37, v36
	v_min_f32_e32 v248, 0xff61b1e6, v32
	v_max_f32_e32 v223, v220, v217
	v_max_f32_e32 v221, v216, v54
	v_min_f32_e32 v246, v239, v245
	v_min_f32_e32 v249, v247, v248
	v_min_f32_e32 v47, v230, v47
	v_max_f32_e32 v230, v236, v240
	v_cmp_ngt_f32_e64 s[16:17], s28, v237
	v_max_f32_e32 v234, v234, v238
	v_cmp_ngt_f32_e64 s[14:15], s28, v233
	v_min_f32_e32 v44, v214, v44
	v_min_f32_e32 v38, v46, v38
	v_min_f32_e32 v42, v42, v43
	v_min_f32_e32 v35, v40, v35
	v_max_f32_e32 v214, v228, v235
	v_max_f32_e32 v36, v37, v36
	v_max_f32_e32 v224, v223, v221
	v_min_f32_e32 v250, v246, v249
	v_min_f32_e32 v39, v226, v39
	v_min_f32_e32 v45, v45, v219
	v_min_f32_e32 v41, v41, v215
	v_cndmask_b32_e64 v236, v199, v237, s[16:17]
	v_cndmask_b32_e64 v238, v199, v233, s[14:15]
	v_max_f32_e32 v46, v44, v38
	v_max_f32_e32 v40, v42, v35
	v_min_f32_e32 v228, v214, v33
	v_min_f32_e32 v37, v36, v32
	v_max_f32_e32 v224, v224, v250
	v_max_f32_e32 v226, v47, v39
	v_max_f32_e32 v215, v45, v41
	v_min_f32_e32 v240, v230, v236
	v_min_f32_e32 v250, v234, v238
	v_min_f32_e32 v218, v225, v218
	v_min_f32_e32 v222, v227, v222
	v_max_f32_e32 v237, v241, v237
	v_max_f32_e32 v233, v243, v233
	v_min_f32_e32 v39, v47, v39
	v_min_f32_e32 v41, v45, v41
	v_max_f32_e32 v47, v230, v236
	v_max_f32_e32 v230, v234, v238
	v_max_f32_e32 v43, v46, v40
	v_min_f32_e32 v235, v228, v37
	v_min_f32_e32 v217, v220, v217
	v_min_f32_e32 v54, v216, v54
	v_max_f32_e32 v239, v239, v245
	v_max_f32_e32 v243, v247, v248
	v_min_f32_e32 v38, v44, v38
	v_min_f32_e32 v35, v42, v35
	v_max_f32_e32 v33, v214, v33
	v_max_f32_e32 v32, v36, v32
	v_max_f32_e32 v219, v226, v215
	v_max_f32_e32 v227, v218, v222
	v_min_f32_e32 v241, v237, v233
	v_max_f32_e32 v45, v39, v41
	v_min_f32_e32 v234, v47, v230
	v_min_f32_e32 v229, v229, v231
	v_max_f32_e32 v231, v242, v244
	v_min_f32_e32 v215, v226, v215
	v_max_f32_e32 v226, v240, v250
	v_min_f32_e32 v251, v240, v250
	v_max_f32_e32 v43, v43, v235
	v_max_f32_e32 v216, v217, v54
	v_min_f32_e32 v245, v239, v243
	v_max_f32_e32 v42, v38, v35
	v_min_f32_e32 v36, v33, v32
	v_min_f32_e32 v221, v223, v221
	v_max_f32_e32 v223, v246, v249
	v_min_f32_e32 v40, v46, v40
	v_max_f32_e32 v37, v228, v37
	v_min_f32_e32 v218, v218, v222
	v_max_f32_e32 v222, v237, v233
	v_min_f32_e32 v54, v217, v54
	v_max_f32_e32 v217, v239, v243
	v_min_f32_e32 v39, v39, v41
	v_max_f32_e32 v41, v47, v230
	v_min_f32_e32 v35, v38, v35
	v_max_f32_e32 v32, v33, v32
	v_max_f32_e32 v227, v227, v241
	v_max_f32_e32 v45, v45, v234
	v_max_f32_e32 v229, v229, v231
	v_max_f32_e32 v215, v215, v226
	v_max_f32_e32 v61, v48, v56
	v_max_f32_e32 v182, v34, v53
	v_max_f32_e32 v219, v219, v251
	v_max_f32_e32 v216, v216, v245
	v_max_f32_e32 v36, v42, v36
	v_max_f32_e32 v221, v221, v223
	v_max_f32_e32 v37, v40, v37
	v_max_f32_e32 v218, v218, v222
	v_max_f32_e32 v217, v54, v217
	v_max_f32_e32 v39, v39, v41
	v_max_f32_e32 v32, v35, v32
	v_max_f32_e32 v49, v50, v52
	v_max_f32_e32 v56, v55, v61
	v_max_f32_e32 v58, v63, v178
	v_max_f32_e32 v60, v180, v182
	v_max_f32_e32 v62, v183, v190
	v_max_f32_e32 v173, v195, v209
	v_max_f32_e32 v179, v210, v211
	v_max_f32_e32 v181, v212, v213
	v_min_f32_e32 v225, v232, v224
	v_min_f32_e32 v241, v219, v43
	v_min_f32_e32 v245, v227, v216
	v_min_f32_e32 v42, v45, v36
	v_min_f32_e32 v223, v229, v221
	v_min_f32_e32 v40, v215, v37
	v_min_f32_e32 v222, v218, v217
	v_min_f32_e32 v33, v39, v32
	v_max_f32_e32 v48, v49, v56
	v_max_f32_e32 v53, v58, v60
	v_max_f32_e32 v57, v62, v173
	v_max_f32_e32 v59, v179, v181
	v_min_f32_e32 v220, v225, v241
	v_min_f32_e32 v44, v245, v42
	v_min_f32_e32 v46, v223, v40
	v_min_f32_e32 v35, v222, v33
	v_max_f32_e32 v34, v48, v53
	v_max_f32_e32 v51, v57, v59
	v_min_f32_e32 v214, v220, v44
	v_min_f32_e32 v38, v46, v35
	v_min_f32_e32 v47, v55, v61
	v_max_f32_e32 v235, v34, v51
	v_min_f32_e32 v41, v214, v38
	v_min_f32_e32 v61, v63, v178
	v_min_f32_e32 v63, v180, v182
	v_max_f32_e32 v54, v235, v41
	v_min_f32_e32 v41, v50, v52
	v_min_f32_e32 v182, v183, v190
	v_min_f32_e32 v183, v195, v209
	v_min_f32_e32 v190, v210, v211
	v_min_f32_e32 v209, v212, v213
	v_max_f32_e32 v212, v232, v224
	v_max_f32_e32 v43, v219, v43
	v_max_f32_e32 v216, v227, v216
	v_max_f32_e32 v36, v45, v36
	v_max_f32_e32 v221, v229, v221
	v_max_f32_e32 v37, v215, v37
	v_max_f32_e32 v217, v218, v217
	v_max_f32_e32 v32, v39, v32
	v_min_f32_e32 v49, v49, v56
	v_min_f32_e32 v224, v58, v60
	v_min_f32_e32 v62, v62, v173
	v_min_f32_e32 v173, v179, v181
	v_max_f32_e32 v181, v225, v241
	v_max_f32_e32 v42, v245, v42
	v_max_f32_e32 v40, v223, v40
	v_max_f32_e32 v33, v222, v33
	v_max_f32_e32 v50, v41, v47
	v_max_f32_e32 v178, v61, v63
	v_max_f32_e32 v195, v182, v183
	v_min_f32_e32 v213, v212, v43
	v_min_f32_e32 v45, v216, v36
	v_min_f32_e32 v215, v221, v37
	v_min_f32_e32 v39, v217, v32
	v_max_f32_e32 v226, v49, v224
	v_max_f32_e32 v179, v62, v173
	v_min_f32_e32 v225, v181, v42
	v_min_f32_e32 v222, v40, v33
	v_min_f32_e32 v41, v41, v47
	v_min_f32_e32 v47, v61, v63
	v_min_f32_e32 v63, v182, v183
	v_min_f32_e32 v182, v190, v209
	v_max_f32_e32 v43, v212, v43
	v_max_f32_e32 v36, v216, v36
	v_max_f32_e32 v37, v221, v37
	v_max_f32_e32 v32, v217, v32
	v_cmp_gt_f32_e64 s[24:25], v63, v182
	v_max_f32_e32 v210, v190, v209
	v_max_f32_e32 v56, v226, v179
	v_min_f32_e32 v58, v225, v222
	v_max_f32_e32 v223, v41, v47
	v_cndmask_b32_e64 v183, v182, v63, s[24:25]
	v_min_f32_e32 v209, v43, v36
	v_min_f32_e32 v212, v37, v32
	v_max_f32_e32 v56, v56, v58
	v_max_f32_e32 v58, v223, v183
	v_min_f32_e32 v60, v209, v212
	v_min_f32_e32 v48, v48, v53
	v_min_f32_e32 v217, v57, v59
	v_max_f32_e32 v44, v220, v44
	v_max_f32_e32 v35, v46, v35
	v_max_f32_e32 v58, v58, v60
	v_max_f32_e32 v53, v48, v217
	v_min_f32_e32 v46, v44, v35
	v_max_f32_e32 v180, v50, v178
	v_min_f32_e32 v219, v213, v45
	v_min_f32_e32 v218, v215, v39
	v_max_f32_e32 v59, v53, v46
	v_min_f32_e32 v46, v50, v178
	v_min_f32_e32 v50, v195, v210
	v_max_f32_e32 v45, v213, v45
	v_max_f32_e32 v39, v215, v39
	v_min_f32_e32 v49, v49, v224
	v_max_f32_e32 v53, v46, v50
	v_min_f32_e32 v57, v45, v39
	v_min_f32_e32 v213, v62, v173
	v_max_f32_e32 v42, v181, v42
	v_max_f32_e32 v33, v40, v33
	v_max_f32_e32 v60, v53, v57
	v_cmp_gt_f32_e64 s[20:21], v49, v213
	v_max_f32_e32 v211, v195, v210
	s_nop 0
	v_cndmask_b32_e64 v57, v213, v49, s[20:21]
	v_min_f32_e32 v40, v42, v33
	v_max_f32_e32 v36, v43, v36
	v_max_f32_e32 v32, v37, v32
	v_max_f32_e32 v61, v57, v40
	v_min_f32_e32 v40, v41, v47
	v_cndmask_b32_e64 v41, v63, v182, s[24:25]
	v_cmp_gt_f32_e64 s[14:15], v40, v41
	v_min_f32_e32 v34, v34, v51
	s_nop 0
	v_cndmask_b32_e64 v47, v41, v40, s[14:15]
	v_min_f32_e32 v37, v36, v32
	s_mov_b64 s[96:97], s[6:7]
	v_max_f32_e32 v62, v47, v37
	v_max_f32_e32 v37, v214, v38
	v_max_f32_e32 v35, v44, v35
	v_min_f32_e32 v55, v219, v218
	v_max_f32_e32 v63, v34, v37
	v_min_f32_e32 v34, v180, v211
	v_max_f32_e32 v37, v219, v218
	v_max_f32_e32 v52, v180, v211
	v_max_f32_e32 v33, v42, v33
	v_max_f32_e32 v173, v34, v37
	v_min_f32_e32 v34, v226, v179
	v_max_f32_e32 v37, v225, v222
	v_max_f32_e32 v32, v36, v32
	v_max_f32_e32 v178, v34, v37
	v_min_f32_e32 v34, v223, v183
	v_max_f32_e32 v37, v209, v212
	v_max_f32_e32 v55, v52, v55
	v_max_f32_e32 v179, v34, v37
	v_min_f32_e32 v34, v48, v217
	v_max_f32_e32 v180, v34, v35
	v_min_f32_e32 v34, v46, v50
	v_max_f32_e32 v35, v45, v39
	v_max_f32_e32 v181, v34, v35
	v_cndmask_b32_e64 v34, v49, v213, s[20:21]
	v_max_f32_e32 v182, v34, v33
	v_cndmask_b32_e64 v33, v40, v41, s[14:15]
	v_min_f32_e32 v52, v54, v55
	v_min_f32_e32 v190, v56, v58
	v_max_f32_e32 v183, v33, v32
	v_min_f32_e32 v53, v59, v60
	v_min_f32_e32 v57, v61, v62
	v_min_f32_e32 v195, v63, v173
	v_min_f32_e32 v209, v178, v179
	v_min_f32_e32 v210, v180, v181
	v_min_f32_e32 v211, v182, v183
	v_min_f32_e32 v216, v52, v190
	v_min_f32_e32 v215, v53, v57
	v_min_f32_e32 v51, v195, v209
	v_min_f32_e32 v50, v210, v211
	s_movk_i32 s10, 0xff
	v_min_f32_e32 v220, v216, v215
	v_min_f32_e32 v212, v51, v50
	s_movk_i32 s8, 0x7f
	v_bitop3_b32 v35, v31, s8, v31 bitop3:0xc
	v_min_f32_e32 v32, v220, v212
	v_and_b32_e32 v33, 0xff, v32
	v_bitop3_b32 v34, v32, s10, v32 bitop3:0xc
	v_cmp_gt_i32_e64 s[6:7], 0, v32
	v_readlane_b32 s94, v255, 39
	v_readlane_b32 s95, v255, 40
	v_cndmask_b32_e64 v213, v34, v33, s[6:7]
	v_and_b32_e32 v33, 0x7f, v31
	v_cmp_gt_i32_e64 s[6:7], 0, v31
	v_and_b32_e32 v34, 15, v213
	v_lshrrev_b32_e32 v214, 4, v213
	v_cndmask_b32_e64 v31, v35, v33, s[6:7]
	v_and_b32_e32 v33, 0x7f, v30
	v_bitop3_b32 v35, v30, s8, v30 bitop3:0xc
	v_cmp_gt_i32_e64 s[6:7], 0, v30
	v_readlane_b32 s86, v255, 31
	v_readlane_b32 s82, v255, 33
	v_cndmask_b32_e64 v30, v35, v33, s[6:7]
	v_and_b32_e32 v33, 0x7f, v29
	v_bitop3_b32 v35, v29, s8, v29 bitop3:0xc
	v_cmp_gt_i32_e64 s[6:7], 0, v29
	v_readlane_b32 s84, v255, 25
	v_readlane_b32 s87, v255, 32
	v_cndmask_b32_e64 v29, v35, v33, s[6:7]
	v_and_b32_e32 v33, 0x7f, v28
	v_bitop3_b32 v35, v28, s8, v28 bitop3:0xc
	v_cmp_gt_i32_e64 s[6:7], 0, v28
	v_readlane_b32 s92, v255, 35
	v_readlane_b32 s88, v255, 29
	v_cndmask_b32_e64 v28, v35, v33, s[6:7]
	v_and_b32_e32 v33, 0x7f, v27
	v_bitop3_b32 v35, v27, s8, v27 bitop3:0xc
	v_cmp_gt_i32_e64 s[6:7], 0, v27
	v_readlane_b32 s90, v255, 27
	v_readlane_b32 s78, v255, 13
	v_cndmask_b32_e64 v27, v35, v33, s[6:7]
	v_and_b32_e32 v33, 0x7f, v26
	v_bitop3_b32 v35, v26, s8, v26 bitop3:0xc
	v_cmp_gt_i32_e64 s[6:7], 0, v26
	v_readlane_b32 s83, v255, 34
	v_readlane_b32 s74, v255, 9
	v_cndmask_b32_e64 v26, v35, v33, s[6:7]
	v_and_b32_e32 v33, 0x7f, v25
	v_bitop3_b32 v35, v25, s8, v25 bitop3:0xc
	v_cmp_gt_i32_e64 s[6:7], 0, v25
	v_readlane_b32 s85, v255, 26
	v_readlane_b32 s76, v255, 11
	v_cndmask_b32_e64 v25, v35, v33, s[6:7]
	v_and_b32_e32 v33, 0x7f, v24
	v_bitop3_b32 v35, v24, s8, v24 bitop3:0xc
	v_cmp_gt_i32_e64 s[6:7], 0, v24
	v_readlane_b32 s22, v255, 23
	v_readlane_b32 s34, v255, 17
	v_cndmask_b32_e64 v24, v35, v33, s[6:7]
	v_and_b32_e32 v33, 0x7f, v23
	v_bitop3_b32 v35, v23, s8, v23 bitop3:0xc
	v_cmp_gt_i32_e64 s[6:7], 0, v23
	v_readlane_b32 s30, v255, 15
	v_readlane_b32 s81, v255, 41
	v_cndmask_b32_e64 v23, v35, v33, s[6:7]
	v_and_b32_e32 v33, 0x7f, v22
	v_bitop3_b32 v35, v22, s8, v22 bitop3:0xc
	v_cmp_gt_i32_e64 s[6:7], 0, v22
	s_movk_i32 s87, 0x4000
	v_readlane_b32 s93, v255, 36
	v_cndmask_b32_e64 v22, v35, v33, s[6:7]
	v_and_b32_e32 v33, 0x7f, v21
	v_bitop3_b32 v35, v21, s8, v21 bitop3:0xc
	v_cmp_gt_i32_e64 s[6:7], 0, v21
	v_readlane_b32 s89, v255, 30
	v_readlane_b32 s91, v255, 28
	v_cndmask_b32_e64 v21, v35, v33, s[6:7]
	v_and_b32_e32 v33, 0x7f, v20
	v_bitop3_b32 v35, v20, s8, v20 bitop3:0xc
	v_cmp_gt_i32_e64 s[6:7], 0, v20
	v_readlane_b32 s79, v255, 14
	v_readlane_b32 s83, v255, 37
	v_cndmask_b32_e64 v20, v35, v33, s[6:7]
	v_and_b32_e32 v33, 0x7f, v19
	v_bitop3_b32 v35, v19, s8, v19 bitop3:0xc
	v_cmp_gt_i32_e64 s[6:7], 0, v19
	v_readlane_b32 s75, v255, 10
	v_readlane_b32 s85, v255, 38
	v_cndmask_b32_e64 v19, v35, v33, s[6:7]
	v_and_b32_e32 v33, 0x7f, v18
	v_bitop3_b32 v35, v18, s8, v18 bitop3:0xc
	v_cmp_gt_i32_e64 s[6:7], 0, v18
	v_readlane_b32 s77, v255, 12
	v_readlane_b32 s23, v255, 24
	v_cndmask_b32_e64 v18, v35, v33, s[6:7]
	v_and_b32_e32 v33, 0x7f, v17
	v_bitop3_b32 v35, v17, s8, v17 bitop3:0xc
	v_cmp_gt_i32_e64 s[6:7], 0, v17
	s_mov_b32 s18, s36
	s_movk_i32 s27, 0x1200
	v_cndmask_b32_e64 v17, v35, v33, s[6:7]
	v_and_b32_e32 v33, 0x7f, v16
	v_bitop3_b32 v35, v16, s8, v16 bitop3:0xc
	v_cmp_gt_i32_e64 s[6:7], 0, v16
	v_readlane_b32 s35, v255, 18
	v_readlane_b32 s31, v255, 16
	v_cndmask_b32_e64 v33, v35, v33, s[6:7]
	v_lshl_add_u32 v252, v34, 8, v207
	ds_read_b32 v16, v252 offset:4096
	v_bitop3_b32 v35, v15, s8, v15 bitop3:0xc
	s_nop 0
	s_nop 1
	s_nop 1
	s_nop 1
	s_nop 1
	s_nop 1
	s_nop 1
	s_nop 1
	s_nop 1
	s_nop 1
	s_nop 1
	s_nop 1
	s_nop 1
	s_nop 1
	s_nop 1
	v_and_b32_e32 v34, 0x7f, v15
	s_nop 0
	s_waitcnt lgkmcnt(0)
	v_and_b32_e32 v252, 0x7f, v16
	v_cmp_gt_i32_e64 s[6:7], 0, v16
	v_xor_b32_e32 v16, 0x7f, v252
	s_nop 0
	v_cndmask_b32_e64 v16, v16, v252, s[6:7]
	v_cmp_gt_i32_e64 s[6:7], 0, v15
	v_and_b32_e32 v15, 0x7f, v14
	s_nop 0
	v_cndmask_b32_e64 v34, v35, v34, s[6:7]
	v_bitop3_b32 v35, v14, s8, v14 bitop3:0xc
	v_cmp_gt_i32_e64 s[6:7], 0, v14
	v_and_b32_e32 v14, 0x7f, v13
	s_nop 0
	v_cndmask_b32_e64 v35, v35, v15, s[6:7]
	v_bitop3_b32 v15, v13, s8, v13 bitop3:0xc
	v_cmp_gt_i32_e64 s[6:7], 0, v13
	v_and_b32_e32 v13, 0x7f, v12
	s_nop 0
	v_cndmask_b32_e64 v36, v15, v14, s[6:7]
	v_bitop3_b32 v14, v12, s8, v12 bitop3:0xc
	v_cmp_gt_i32_e64 s[6:7], 0, v12
	v_and_b32_e32 v12, 0x7f, v11
	v_max_f32_e32 v15, v59, v60
	v_cndmask_b32_e64 v37, v14, v13, s[6:7]
	v_bitop3_b32 v13, v11, s8, v11 bitop3:0xc
	v_cmp_gt_i32_e64 s[6:7], 0, v11
	v_and_b32_e32 v11, 0x7f, v10
	v_max_f32_e32 v14, v56, v58
	v_cndmask_b32_e64 v38, v13, v12, s[6:7]
	v_bitop3_b32 v12, v10, s8, v10 bitop3:0xc
	v_cmp_gt_i32_e64 s[6:7], 0, v10
	v_and_b32_e32 v10, 0x7f, v9
	v_max_f32_e32 v59, v61, v62
	v_cndmask_b32_e64 v39, v12, v11, s[6:7]
	v_bitop3_b32 v11, v9, s8, v9 bitop3:0xc
	v_cmp_gt_i32_e64 s[6:7], 0, v9
	v_and_b32_e32 v9, 0x7f, v8
	v_max_f32_e32 v60, v63, v173
	v_cndmask_b32_e64 v40, v11, v10, s[6:7]
	v_bitop3_b32 v10, v8, s8, v8 bitop3:0xc
	v_cmp_gt_i32_e64 s[6:7], 0, v8
	v_and_b32_e32 v8, 0x7f, v7
	v_max_f32_e32 v61, v178, v179
	v_cndmask_b32_e64 v41, v10, v9, s[6:7]
	v_bitop3_b32 v9, v7, s8, v7 bitop3:0xc
	v_cmp_gt_i32_e64 s[6:7], 0, v7
	v_and_b32_e32 v7, 0x7f, v6
	v_max_f32_e32 v62, v180, v181
	v_cndmask_b32_e64 v42, v9, v8, s[6:7]
	v_bitop3_b32 v8, v6, s8, v6 bitop3:0xc
	v_cmp_gt_i32_e64 s[6:7], 0, v6
	v_and_b32_e32 v6, 0x7f, v5
	v_max_f32_e32 v9, v210, v211
	v_cndmask_b32_e64 v43, v8, v7, s[6:7]
	v_bitop3_b32 v7, v5, s8, v5 bitop3:0xc
	v_cmp_gt_i32_e64 s[6:7], 0, v5
	v_and_b32_e32 v5, 0x7f, v4
	v_max_f32_e32 v8, v195, v209
	v_cndmask_b32_e64 v44, v7, v6, s[6:7]
	v_bitop3_b32 v6, v4, s8, v4 bitop3:0xc
	v_cmp_gt_i32_e64 s[6:7], 0, v4
	v_and_b32_e32 v4, 0x7f, v3
	v_max_f32_e32 v63, v182, v183
	v_cndmask_b32_e64 v45, v6, v5, s[6:7]
	v_bitop3_b32 v5, v3, s8, v3 bitop3:0xc
	v_cmp_gt_i32_e64 s[6:7], 0, v3
	v_and_b32_e32 v3, 0x7f, v2
	s_nop 0
	v_cndmask_b32_e64 v46, v5, v4, s[6:7]
	v_bitop3_b32 v4, v2, s8, v2 bitop3:0xc
	v_cmp_gt_i32_e64 s[6:7], 0, v2
	v_and_b32_e32 v2, 0x7f, v1
	s_nop 0
	v_cndmask_b32_e64 v47, v4, v3, s[6:7]
	v_bitop3_b32 v3, v1, s8, v1 bitop3:0xc
	v_cmp_gt_i32_e64 s[6:7], 0, v1
	v_and_b32_e32 v1, 0x7f, v0
	v_max_f32_e32 v4, v51, v50
	v_cndmask_b32_e64 v48, v3, v2, s[6:7]
	v_bitop3_b32 v2, v0, s8, v0 bitop3:0xc
	v_cmp_gt_i32_e64 s[6:7], 0, v0
	v_min_f32_e32 v56, v60, v61
	s_nop 0
	v_cndmask_b32_e64 v49, v2, v1, s[6:7]
	v_lshl_add_u32 v252, v214, 8, v207
	ds_read_b32 v0, v252
	v_min_f32_e32 v58, v62, v63
	s_nop 0
	v_max_f32_e32 v60, v60, v61
	v_max_f32_e32 v61, v62, v63
	v_readlane_b32 s46, v255, 21
	v_readlane_b32 s44, v255, 19
	v_readlane_b32 s47, v255, 22
	v_readlane_b32 s45, v255, 20
	s_nop 1
	s_nop 1
	s_nop 1
	s_nop 1
	s_nop 1
	s_nop 1
	s_nop 1
	s_nop 1
	s_nop 1
	s_nop 1
	s_nop 1
	s_nop 1
	s_waitcnt lgkmcnt(0)
	v_and_b32_e32 v252, 0x7f, v0
	v_cmp_gt_i32_e64 s[6:7], 0, v0
	v_xor_b32_e32 v0, 0x7f, v252
	s_nop 0
	v_cndmask_b32_e64 v3, v0, v252, s[6:7]
	v_max_f32_e32 v0, v220, v212
	v_and_b32_e32 v1, 0xff, v0
	v_bitop3_b32 v2, v0, s10, v0 bitop3:0xc
	v_cmp_gt_i32_e64 s[6:7], 0, v0
	v_and_b32_e32 v12, 0xffffff00, v0
	v_lshl_add_u32 v3, v3, 7, v16
	v_cndmask_b32_e64 v0, v2, v1, s[6:7]
	v_lshrrev_b32_e32 v1, 4, v0
	v_lshl_add_u32 v252, v1, 8, v207
	ds_read_b32 v2, v252
	v_and_b32_e32 v0, 15, v0
	s_nop 0
	s_nop 1
	s_nop 1
	s_nop 1
	s_nop 1
	s_nop 1
	s_nop 1
	s_nop 1
	s_nop 1
	s_nop 1
	s_nop 1
	s_nop 1
	s_nop 1
	s_nop 1
	s_nop 1
	s_nop 1
	s_waitcnt lgkmcnt(0)
	v_and_b32_e32 v252, 0x7f, v2
	v_cmp_gt_i32_e64 s[6:7], 0, v2
	v_xor_b32_e32 v2, 0x7f, v252
	s_nop 0
	v_cndmask_b32_e64 v1, v2, v252, s[6:7]
	v_lshl_add_u32 v252, v0, 8, v207
	ds_read_b32 v2, v252 offset:4096
	s_nop 1
	s_nop 1
	s_nop 1
	s_nop 1
	s_nop 1
	s_nop 1
	s_nop 1
	s_nop 1
	s_nop 1
	s_nop 1
	s_nop 1
	s_nop 1
	s_nop 1
	s_nop 1
	s_nop 1
	s_nop 1
	s_waitcnt lgkmcnt(0)
	v_and_b32_e32 v252, 0x7f, v2
	v_cmp_gt_i32_e64 s[6:7], 0, v2
	v_xor_b32_e32 v2, 0x7f, v252
	s_nop 0
	v_cndmask_b32_e64 v0, v2, v252, s[6:7]
	v_lshl_add_u32 v2, v1, 7, v0
	v_max_f32_e32 v0, v216, v215
	v_min_f32_e32 v1, v0, v4
	v_and_b32_e32 v5, 0xff, v1
	v_bitop3_b32 v6, v1, s10, v1 bitop3:0xc
	v_cmp_gt_i32_e64 s[8:9], 0, v1
	v_and_b32_e32 v50, 0xffffff00, v1
	v_max_f32_e32 v0, v0, v4
	v_cndmask_b32_e64 v1, v6, v5, s[8:9]
	v_lshrrev_b32_e32 v5, 4, v1
	v_lshl_add_u32 v252, v5, 8, v207
	ds_read_b32 v6, v252
	v_and_b32_e32 v1, 15, v1
	v_and_b32_e32 v4, 0xff, v0
	v_cmp_gt_i32_e64 s[6:7], 0, v0
	v_and_b32_e32 v51, 0xffffff00, v0
	s_nop 1
	s_nop 1
	s_nop 1
	s_nop 1
	s_nop 1
	s_nop 1
	s_nop 1
	s_nop 1
	s_nop 1
	s_nop 1
	s_nop 1
	s_nop 1
	s_nop 1
	s_nop 1
	s_waitcnt lgkmcnt(0)
	v_and_b32_e32 v252, 0x7f, v6
	v_cmp_gt_i32_e64 s[8:9], 0, v6
	v_xor_b32_e32 v6, 0x7f, v252
	s_nop 0
	v_cndmask_b32_e64 v5, v6, v252, s[8:9]
	v_lshl_add_u32 v252, v1, 8, v207
	ds_read_b32 v6, v252 offset:4096
	s_nop 1
	s_nop 1
	s_nop 1
	s_nop 1
	s_nop 1
	s_nop 1
	s_nop 1
	s_nop 1
	s_nop 1
	s_nop 1
	s_nop 1
	s_nop 1
	s_nop 1
	s_nop 1
	s_nop 1
	s_nop 1
	s_waitcnt lgkmcnt(0)
	v_and_b32_e32 v252, 0x7f, v6
	v_cmp_gt_i32_e64 s[8:9], 0, v6
	v_xor_b32_e32 v6, 0x7f, v252
	s_nop 0
	v_cndmask_b32_e64 v1, v6, v252, s[8:9]
	v_lshl_add_u32 v1, v5, 7, v1
	v_bitop3_b32 v5, v0, s10, v0 bitop3:0xc
	v_cndmask_b32_e64 v0, v5, v4, s[6:7]
	v_lshrrev_b32_e32 v4, 4, v0
	v_lshl_add_u32 v252, v4, 8, v207
	ds_read_b32 v5, v252
	v_and_b32_e32 v0, 15, v0
	s_nop 0
	s_nop 1
	s_nop 1
	s_nop 1
	s_nop 1
	s_nop 1
	s_nop 1
	s_nop 1
	s_nop 1
	s_nop 1
	s_nop 1
	s_nop 1
	s_nop 1
	s_nop 1
	s_nop 1
	s_nop 1
	s_waitcnt lgkmcnt(0)
	v_and_b32_e32 v252, 0x7f, v5
	v_cmp_gt_i32_e64 s[6:7], 0, v5
	v_xor_b32_e32 v5, 0x7f, v252
	s_nop 0
	v_cndmask_b32_e64 v4, v5, v252, s[6:7]
	v_lshl_add_u32 v252, v0, 8, v207
	ds_read_b32 v5, v252 offset:4096
	s_nop 1
	s_nop 1
	s_nop 1
	s_nop 1
	s_nop 1
	s_nop 1
	s_nop 1
	s_nop 1
	s_nop 1
	s_nop 1
	s_nop 1
	s_nop 1
	s_nop 1
	s_nop 1
	s_nop 1
	s_nop 1
	s_waitcnt lgkmcnt(0)
	v_and_b32_e32 v252, 0x7f, v5
	v_cmp_gt_i32_e64 s[6:7], 0, v5
	v_xor_b32_e32 v5, 0x7f, v252
	s_nop 0
	v_cndmask_b32_e64 v0, v5, v252, s[6:7]
	v_lshl_add_u32 v0, v4, 7, v0
	v_max_f32_e32 v4, v52, v190
	v_max_f32_e32 v5, v53, v57
	v_min_f32_e32 v6, v4, v5
	v_min_f32_e32 v10, v8, v9
	v_max_f32_e32 v4, v4, v5
	v_max_f32_e32 v8, v8, v9
	v_min_f32_e32 v7, v6, v10
	v_and_b32_e32 v11, 0xff, v7
	v_bitop3_b32 v13, v7, s10, v7 bitop3:0xc
	v_cmp_gt_i32_e64 s[8:9], 0, v7
	v_and_b32_e32 v52, 0xffffff00, v7
	v_max_f32_e32 v6, v6, v10
	v_cndmask_b32_e64 v7, v13, v11, s[8:9]
	v_lshrrev_b32_e32 v11, 4, v7
	v_lshl_add_u32 v252, v11, 8, v207
	ds_read_b32 v13, v252
	v_and_b32_e32 v7, 15, v7
	v_and_b32_e32 v10, 0xff, v6
	v_cmp_gt_i32_e64 s[6:7], 0, v6
	v_and_b32_e32 v53, 0xffffff00, v6
	s_nop 1
	s_nop 1
	s_nop 1
	s_nop 1
	s_nop 1
	s_nop 1
	s_nop 1
	s_nop 1
	s_nop 1
	s_nop 1
	s_nop 1
	s_nop 1
	s_nop 1
	s_nop 1
	s_waitcnt lgkmcnt(0)
	v_and_b32_e32 v252, 0x7f, v13
	v_cmp_gt_i32_e64 s[8:9], 0, v13
	v_xor_b32_e32 v13, 0x7f, v252
	s_nop 0
	v_cndmask_b32_e64 v11, v13, v252, s[8:9]
	v_lshl_add_u32 v252, v7, 8, v207
	ds_read_b32 v13, v252 offset:4096
	s_nop 1
	s_nop 1
	s_nop 1
	s_nop 1
	s_nop 1
	s_nop 1
	s_nop 1
	s_nop 1
	s_nop 1
	s_nop 1
	s_nop 1
	s_nop 1
	s_nop 1
	s_nop 1
	s_nop 1
	s_nop 1
	s_waitcnt lgkmcnt(0)
	v_and_b32_e32 v252, 0x7f, v13
	v_cmp_gt_i32_e64 s[8:9], 0, v13
	v_xor_b32_e32 v13, 0x7f, v252
	s_nop 0
	v_cndmask_b32_e64 v7, v13, v252, s[8:9]
	v_lshl_add_u32 v7, v11, 7, v7
	v_bitop3_b32 v11, v6, s10, v6 bitop3:0xc
	v_cndmask_b32_e64 v6, v11, v10, s[6:7]
	v_lshrrev_b32_e32 v10, 4, v6
	v_lshl_add_u32 v252, v10, 8, v207
	ds_read_b32 v11, v252
	v_and_b32_e32 v6, 15, v6
	v_max_f32_e32 v13, v54, v55
	v_min_f32_e32 v55, v56, v58
	s_nop 0
	v_max_f32_e32 v58, v56, v58
	s_nop 0
	s_nop 1
	s_nop 1
	s_nop 1
	s_nop 1
	s_nop 1
	s_nop 1
	s_nop 1
	s_nop 1
	s_nop 1
	s_nop 1
	s_nop 1
	s_nop 1
	s_nop 1
	s_waitcnt lgkmcnt(0)
	v_and_b32_e32 v252, 0x7f, v11
	v_cmp_gt_i32_e64 s[6:7], 0, v11
	v_xor_b32_e32 v11, 0x7f, v252
	s_nop 0
	v_cndmask_b32_e64 v10, v11, v252, s[6:7]
	v_lshl_add_u32 v252, v6, 8, v207
	ds_read_b32 v11, v252 offset:4096
	s_nop 1
	s_nop 1
	s_nop 1
	s_nop 1
	s_nop 1
	s_nop 1
	s_nop 1
	s_nop 1
	s_nop 1
	s_nop 1
	s_nop 1
	s_nop 1
	s_nop 1
	s_nop 1
	s_nop 1
	s_nop 1
	s_waitcnt lgkmcnt(0)
	v_and_b32_e32 v252, 0x7f, v11
	v_cmp_gt_i32_e64 s[6:7], 0, v11
	v_xor_b32_e32 v11, 0x7f, v252
	s_nop 0
	v_cndmask_b32_e64 v6, v11, v252, s[6:7]
	v_lshl_add_u32 v6, v10, 7, v6
	v_min_f32_e32 v5, v4, v8
	v_and_b32_e32 v9, 0xff, v5
	v_bitop3_b32 v10, v5, s10, v5 bitop3:0xc
	v_cmp_gt_i32_e64 s[8:9], 0, v5
	v_and_b32_e32 v57, 0xffffff00, v5
	v_max_f32_e32 v4, v4, v8
	v_cndmask_b32_e64 v5, v10, v9, s[8:9]
	v_lshrrev_b32_e32 v9, 4, v5
	v_lshl_add_u32 v252, v9, 8, v207
	ds_read_b32 v10, v252
	v_and_b32_e32 v5, 15, v5
	v_and_b32_e32 v8, 0xff, v4
	v_cmp_gt_i32_e64 s[6:7], 0, v4
	v_and_b32_e32 v209, 0xffffff00, v4
	s_nop 1
	s_nop 1
	s_nop 1
	s_nop 1
	s_nop 1
	s_nop 1
	s_nop 1
	s_nop 1
	s_nop 1
	s_nop 1
	s_nop 1
	s_nop 1
	s_nop 1
	s_nop 1
	s_waitcnt lgkmcnt(0)
	v_and_b32_e32 v252, 0x7f, v10
	v_cmp_gt_i32_e64 s[8:9], 0, v10
	v_xor_b32_e32 v10, 0x7f, v252
	s_nop 0
	v_cndmask_b32_e64 v9, v10, v252, s[8:9]
	v_lshl_add_u32 v252, v5, 8, v207
	ds_read_b32 v10, v252 offset:4096
	s_nop 1
	s_nop 1
	s_nop 1
	s_nop 1
	s_nop 1
	s_nop 1
	s_nop 1
	s_nop 1
	s_nop 1
	s_nop 1
	s_nop 1
	s_nop 1
	s_nop 1
	s_nop 1
	s_nop 1
	s_nop 1
	s_waitcnt lgkmcnt(0)
	v_and_b32_e32 v252, 0x7f, v10
	v_cmp_gt_i32_e64 s[8:9], 0, v10
	v_xor_b32_e32 v10, 0x7f, v252
	s_nop 0
	v_cndmask_b32_e64 v5, v10, v252, s[8:9]
	v_lshl_add_u32 v5, v9, 7, v5
	v_bitop3_b32 v9, v4, s10, v4 bitop3:0xc
	v_cndmask_b32_e64 v4, v9, v8, s[6:7]
	v_lshrrev_b32_e32 v8, 4, v4
	v_lshl_add_u32 v252, v8, 8, v207
	ds_read_b32 v9, v252
	v_and_b32_e32 v4, 15, v4
	s_nop 0
	s_nop 1
	s_nop 1
	s_nop 1
	s_nop 1
	s_nop 1
	s_nop 1
	s_nop 1
	s_nop 1
	s_nop 1
	s_nop 1
	s_nop 1
	s_nop 1
	s_nop 1
	s_nop 1
	s_nop 1
	s_waitcnt lgkmcnt(0)
	v_and_b32_e32 v252, 0x7f, v9
	v_cmp_gt_i32_e64 s[6:7], 0, v9
	v_xor_b32_e32 v9, 0x7f, v252
	s_nop 0
	v_cndmask_b32_e64 v8, v9, v252, s[6:7]
	v_lshl_add_u32 v252, v4, 8, v207
	ds_read_b32 v9, v252 offset:4096
	s_nop 1
	s_nop 1
	s_nop 1
	s_nop 1
	s_nop 1
	s_nop 1
	s_nop 1
	s_nop 1
	s_nop 1
	s_nop 1
	s_nop 1
	s_nop 1
	s_nop 1
	s_nop 1
	s_nop 1
	s_nop 1
	s_waitcnt lgkmcnt(0)
	v_and_b32_e32 v252, 0x7f, v9
	v_cmp_gt_i32_e64 s[6:7], 0, v9
	v_xor_b32_e32 v9, 0x7f, v252
	s_nop 0
	v_cndmask_b32_e64 v4, v9, v252, s[6:7]
	v_lshl_add_u32 v4, v8, 7, v4
	v_min_f32_e32 v8, v13, v14
	v_min_f32_e32 v9, v15, v59
	v_max_f32_e32 v13, v13, v14
	v_max_f32_e32 v59, v15, v59
	v_min_f32_e32 v10, v8, v9
	v_max_f32_e32 v8, v8, v9
	v_min_f32_e32 v11, v10, v55
	v_and_b32_e32 v173, 0xff, v11
	v_bitop3_b32 v178, v11, s10, v11 bitop3:0xc
	v_cmp_gt_i32_e64 s[8:9], 0, v11
	v_and_b32_e32 v54, 0xffffff00, v11
	v_max_f32_e32 v10, v10, v55
	v_cndmask_b32_e64 v11, v178, v173, s[8:9]
	v_lshrrev_b32_e32 v173, 4, v11
	v_lshl_add_u32 v252, v173, 8, v207
	ds_read_b32 v178, v252
	v_and_b32_e32 v11, 15, v11
	v_cmp_gt_i32_e64 s[6:7], 0, v10
	v_and_b32_e32 v55, 0xffffff00, v10
	s_nop 0
	v_min_f32_e32 v14, v13, v59
	v_min_f32_e32 v62, v60, v61
	v_max_f32_e32 v59, v13, v59
	v_max_f32_e32 v60, v60, v61
	s_nop 0
	s_nop 0
	v_min_f32_e32 v13, v59, v60
	v_and_b32_e32 v61, 0xffffff00, v13
	v_max_f32_e32 v59, v59, v60
	v_cmp_gt_i32_e32 vcc, 0, v59
	v_and_b32_e32 v60, 0xffffff00, v59
	v_sub_f32_e32 v12, v12, v60
	v_mul_f32_e32 v12, 0x3fb8aa3b, v12
	s_nop 0
	s_nop 1
	s_nop 1
	s_nop 1
	s_nop 1
	s_nop 1
	s_nop 1
	s_nop 1
	s_waitcnt lgkmcnt(0)
	v_and_b32_e32 v252, 0x7f, v178
	v_cmp_gt_i32_e64 s[8:9], 0, v178
	v_xor_b32_e32 v178, 0x7f, v252
	s_nop 0
	v_cndmask_b32_e64 v173, v178, v252, s[8:9]
	v_lshl_add_u32 v252, v11, 8, v207
	ds_read_b32 v178, v252 offset:4096
	s_nop 1
	s_nop 1
	s_nop 1
	s_nop 1
	s_nop 1
	s_nop 1
	s_nop 1
	s_nop 1
	s_nop 1
	s_nop 1
	s_nop 1
	s_nop 1
	s_nop 1
	s_nop 1
	s_nop 1
	s_nop 1
	s_waitcnt lgkmcnt(0)
	v_and_b32_e32 v252, 0x7f, v178
	v_cmp_gt_i32_e64 s[8:9], 0, v178
	v_xor_b32_e32 v178, 0x7f, v252
	s_nop 0
	v_cndmask_b32_e64 v11, v178, v252, s[8:9]
	v_lshl_add_u32 v11, v173, 7, v11
	v_and_b32_e32 v173, 0xff, v10
	v_bitop3_b32 v178, v10, s10, v10 bitop3:0xc
	v_cndmask_b32_e64 v10, v178, v173, s[6:7]
	v_lshrrev_b32_e32 v173, 4, v10
	v_lshl_add_u32 v252, v173, 8, v207
	ds_read_b32 v178, v252
	v_and_b32_e32 v10, 15, v10
	s_nop 0
	s_nop 1
	s_nop 1
	s_nop 1
	s_nop 1
	s_nop 1
	s_nop 1
	s_nop 1
	s_nop 1
	s_nop 1
	s_nop 1
	s_nop 1
	s_nop 1
	s_nop 1
	s_nop 1
	s_nop 1
	s_waitcnt lgkmcnt(0)
	v_and_b32_e32 v252, 0x7f, v178
	v_cmp_gt_i32_e64 s[6:7], 0, v178
	v_xor_b32_e32 v178, 0x7f, v252
	s_nop 0
	v_cndmask_b32_e64 v173, v178, v252, s[6:7]
	v_lshl_add_u32 v252, v10, 8, v207
	ds_read_b32 v178, v252 offset:4096
	s_nop 1
	s_nop 1
	s_nop 1
	s_nop 1
	s_nop 1
	s_nop 1
	s_nop 1
	s_nop 1
	s_nop 1
	s_nop 1
	s_nop 1
	s_nop 1
	s_nop 1
	s_nop 1
	s_nop 1
	s_nop 1
	s_waitcnt lgkmcnt(0)
	v_and_b32_e32 v252, 0x7f, v178
	v_cmp_gt_i32_e64 s[6:7], 0, v178
	v_xor_b32_e32 v178, 0x7f, v252
	s_nop 0
	v_cndmask_b32_e64 v10, v178, v252, s[6:7]
	v_lshl_add_u32 v10, v173, 7, v10
	v_min_f32_e32 v9, v8, v58
	v_and_b32_e32 v173, 0xff, v9
	v_bitop3_b32 v178, v9, s10, v9 bitop3:0xc
	v_cmp_gt_i32_e64 s[8:9], 0, v9
	v_and_b32_e32 v56, 0xffffff00, v9
	v_max_f32_e32 v8, v8, v58
	v_cndmask_b32_e64 v9, v178, v173, s[8:9]
	v_lshrrev_b32_e32 v173, 4, v9
	v_lshl_add_u32 v252, v173, 8, v207
	ds_read_b32 v178, v252
	v_and_b32_e32 v9, 15, v9
	v_cmp_gt_i32_e64 s[6:7], 0, v8
	v_and_b32_e32 v58, 0xffffff00, v8
	s_nop 0
	s_nop 1
	s_nop 1
	s_nop 1
	s_nop 1
	s_nop 1
	s_nop 1
	s_nop 1
	s_nop 1
	s_nop 1
	s_nop 1
	s_nop 1
	s_nop 1
	s_nop 1
	s_nop 1
	s_waitcnt lgkmcnt(0)
	v_and_b32_e32 v252, 0x7f, v178
	v_cmp_gt_i32_e64 s[8:9], 0, v178
	v_xor_b32_e32 v178, 0x7f, v252
	s_nop 0
	v_cndmask_b32_e64 v173, v178, v252, s[8:9]
	v_lshl_add_u32 v252, v9, 8, v207
	ds_read_b32 v178, v252 offset:4096
	s_nop 1
	s_nop 1
	s_nop 1
	s_nop 1
	s_nop 1
	s_nop 1
	s_nop 1
	s_nop 1
	s_nop 1
	s_nop 1
	s_nop 1
	s_nop 1
	s_nop 1
	s_nop 1
	s_nop 1
	s_nop 1
	s_waitcnt lgkmcnt(0)
	v_and_b32_e32 v252, 0x7f, v178
	v_cmp_gt_i32_e64 s[8:9], 0, v178
	v_xor_b32_e32 v178, 0x7f, v252
	s_nop 0
	v_cndmask_b32_e64 v9, v178, v252, s[8:9]
	v_lshl_add_u32 v9, v173, 7, v9
	v_and_b32_e32 v173, 0xff, v8
	v_bitop3_b32 v178, v8, s10, v8 bitop3:0xc
	v_cndmask_b32_e64 v8, v178, v173, s[6:7]
	v_lshrrev_b32_e32 v173, 4, v8
	v_lshl_add_u32 v252, v173, 8, v207
	ds_read_b32 v178, v252
	v_and_b32_e32 v8, 15, v8
	s_nop 0
	s_nop 1
	s_nop 1
	s_nop 1
	s_nop 1
	s_nop 1
	s_nop 1
	s_nop 1
	s_nop 1
	s_nop 1
	s_nop 1
	s_nop 1
	s_nop 1
	s_nop 1
	s_nop 1
	s_nop 1
	s_waitcnt lgkmcnt(0)
	v_and_b32_e32 v252, 0x7f, v178
	v_cmp_gt_i32_e64 s[6:7], 0, v178
	v_xor_b32_e32 v178, 0x7f, v252
	s_nop 0
	v_cndmask_b32_e64 v173, v178, v252, s[6:7]
	v_lshl_add_u32 v252, v8, 8, v207
	ds_read_b32 v178, v252 offset:4096
	s_nop 1
	s_nop 1
	s_nop 1
	s_nop 1
	s_nop 1
	s_nop 1
	s_nop 1
	s_nop 1
	s_nop 1
	s_nop 1
	s_nop 1
	s_nop 1
	s_nop 1
	s_nop 1
	s_nop 1
	s_nop 1
	s_waitcnt lgkmcnt(0)
	v_and_b32_e32 v252, 0x7f, v178
	v_cmp_gt_i32_e64 s[6:7], 0, v178
	v_xor_b32_e32 v178, 0x7f, v252
	s_nop 0
	v_cndmask_b32_e64 v8, v178, v252, s[6:7]
	v_lshl_add_u32 v8, v173, 7, v8
	v_min_f32_e32 v15, v14, v62
	v_and_b32_e32 v173, 0xff, v15
	v_bitop3_b32 v178, v15, s10, v15 bitop3:0xc
	v_cmp_gt_i32_e64 s[8:9], 0, v15
	v_and_b32_e32 v63, 0xffffff00, v15
	v_max_f32_e32 v14, v14, v62
	v_cndmask_b32_e64 v15, v178, v173, s[8:9]
	v_lshrrev_b32_e32 v173, 4, v15
	v_lshl_add_u32 v252, v173, 8, v207
	ds_read_b32 v178, v252
	v_and_b32_e32 v15, 15, v15
	v_cmp_gt_i32_e64 s[6:7], 0, v14
	v_and_b32_e32 v62, 0xffffff00, v14
	s_nop 0
	s_nop 1
	s_nop 1
	s_nop 1
	s_nop 1
	s_nop 1
	s_nop 1
	s_nop 1
	s_nop 1
	s_nop 1
	s_nop 1
	s_nop 1
	s_nop 1
	s_nop 1
	s_nop 1
	s_waitcnt lgkmcnt(0)
	v_and_b32_e32 v252, 0x7f, v178
	v_cmp_gt_i32_e64 s[8:9], 0, v178
	v_xor_b32_e32 v178, 0x7f, v252
	s_nop 0
	v_cndmask_b32_e64 v173, v178, v252, s[8:9]
	v_lshl_add_u32 v252, v15, 8, v207
	ds_read_b32 v178, v252 offset:4096
	s_nop 1
	s_nop 1
	s_nop 1
	s_nop 1
	s_nop 1
	s_nop 1
	s_nop 1
	s_nop 1
	s_nop 1
	s_nop 1
	s_nop 1
	s_nop 1
	s_nop 1
	s_nop 1
	s_nop 1
	s_nop 1
	s_waitcnt lgkmcnt(0)
	v_and_b32_e32 v252, 0x7f, v178
	v_cmp_gt_i32_e64 s[8:9], 0, v178
	v_xor_b32_e32 v178, 0x7f, v252
	s_nop 0
	v_cndmask_b32_e64 v15, v178, v252, s[8:9]
	v_lshl_add_u32 v15, v173, 7, v15
	v_and_b32_e32 v173, 0xff, v14
	v_bitop3_b32 v178, v14, s10, v14 bitop3:0xc
	v_cndmask_b32_e64 v14, v178, v173, s[6:7]
	v_lshrrev_b32_e32 v173, 4, v14
	v_lshl_add_u32 v252, v173, 8, v207
	ds_read_b32 v178, v252
	v_and_b32_e32 v14, 15, v14
	v_readlane_b32 s8, v253, 23
	v_readlane_b32 s9, v253, 24
	s_nop 0
	s_nop 1
	s_nop 1
	s_nop 1
	s_nop 1
	s_nop 1
	s_nop 1
	s_nop 1
	s_nop 1
	s_nop 1
	s_nop 1
	s_nop 1
	s_nop 1
	s_nop 1
	s_nop 1
	s_waitcnt lgkmcnt(0)
	v_and_b32_e32 v252, 0x7f, v178
	v_cmp_gt_i32_e64 s[6:7], 0, v178
	v_xor_b32_e32 v178, 0x7f, v252
	s_nop 0
	v_cndmask_b32_e64 v173, v178, v252, s[6:7]
	v_lshl_add_u32 v252, v14, 8, v207
	ds_read_b32 v178, v252 offset:4096
	s_nop 1
	s_nop 1
	s_nop 1
	s_nop 1
	s_nop 1
	s_nop 1
	s_nop 1
	s_nop 1
	s_nop 1
	s_nop 1
	s_nop 1
	s_nop 1
	s_nop 1
	s_nop 1
	s_nop 1
	s_nop 1
	s_waitcnt lgkmcnt(0)
	v_and_b32_e32 v252, 0x7f, v178
	v_cmp_gt_i32_e64 s[6:7], 0, v178
	v_xor_b32_e32 v178, 0x7f, v252
	s_nop 0
	v_cndmask_b32_e64 v14, v178, v252, s[6:7]
	v_lshl_add_u32 v14, v173, 7, v14
	v_and_b32_e32 v173, 0xff, v13
	v_bitop3_b32 v178, v13, s10, v13 bitop3:0xc
	v_cmp_gt_i32_e64 s[6:7], 0, v13
	s_nop 1
	v_cndmask_b32_e64 v13, v178, v173, s[6:7]
	v_lshrrev_b32_e32 v173, 4, v13
	v_lshl_add_u32 v252, v173, 8, v207
	ds_read_b32 v178, v252
	v_and_b32_e32 v13, 15, v13
	s_nop 0
	s_nop 1
	s_nop 1
	s_nop 1
	s_nop 1
	s_nop 1
	s_nop 1
	s_nop 1
	s_nop 1
	s_nop 1
	s_nop 1
	s_nop 1
	s_nop 1
	s_nop 1
	s_nop 1
	s_nop 1
	s_waitcnt lgkmcnt(0)
	v_and_b32_e32 v252, 0x7f, v178
	v_cmp_gt_i32_e64 s[6:7], 0, v178
	v_xor_b32_e32 v178, 0x7f, v252
	s_nop 0
	v_cndmask_b32_e64 v173, v178, v252, s[6:7]
	v_lshl_add_u32 v252, v13, 8, v207
	ds_read_b32 v178, v252 offset:4096
	s_nop 1
	s_nop 1
	s_nop 1
	s_nop 1
	s_nop 1
	s_nop 1
	s_nop 1
	s_nop 1
	s_nop 1
	s_nop 1
	s_nop 1
	s_nop 1
	s_nop 1
	s_nop 1
	s_nop 1
	s_nop 1
	s_waitcnt lgkmcnt(0)
	v_and_b32_e32 v252, 0x7f, v178
	v_cmp_gt_i32_e64 s[6:7], 0, v178
	v_xor_b32_e32 v178, 0x7f, v252
	s_nop 0
	v_cndmask_b32_e64 v13, v178, v252, s[6:7]
	v_lshl_add_u32 v13, v173, 7, v13
	v_and_b32_e32 v173, 0xff, v59
	v_bitop3_b32 v178, v59, s10, v59 bitop3:0xc
	v_cndmask_b32_e32 v59, v178, v173, vcc
	v_lshrrev_b32_e32 v173, 4, v59
	v_cmp_gt_u32_e32 vcc, 16, v59
	s_nop 1
	v_cndmask_b32_e32 v49, 0, v49, vcc
	v_cmp_eq_u32_e32 vcc, 1, v173
	s_nop 1
	v_cndmask_b32_e32 v48, v49, v48, vcc
	v_cmp_eq_u32_e32 vcc, 2, v173
	s_nop 1
	v_cndmask_b32_e32 v47, v48, v47, vcc
	v_cmp_eq_u32_e32 vcc, 3, v173
	s_nop 1
	v_cndmask_b32_e32 v46, v47, v46, vcc
	v_cmp_eq_u32_e32 vcc, 4, v173
	s_nop 1
	v_cndmask_b32_e32 v45, v46, v45, vcc
	v_cmp_eq_u32_e32 vcc, 5, v173
	s_nop 1
	v_cndmask_b32_e32 v44, v45, v44, vcc
	v_cmp_eq_u32_e32 vcc, 6, v173
	s_nop 1
	v_cndmask_b32_e32 v43, v44, v43, vcc
	v_cmp_eq_u32_e32 vcc, 7, v173
	s_nop 1
	v_cndmask_b32_e32 v42, v43, v42, vcc
	v_cmp_eq_u32_e32 vcc, 8, v173
	s_nop 1
	v_cndmask_b32_e32 v41, v42, v41, vcc
	v_cmp_eq_u32_e32 vcc, 9, v173
	s_nop 1
	v_cndmask_b32_e32 v40, v41, v40, vcc
	v_cmp_eq_u32_e32 vcc, 10, v173
	s_nop 1
	v_cndmask_b32_e32 v39, v40, v39, vcc
	v_cmp_eq_u32_e32 vcc, 11, v173
	s_nop 1
	v_cndmask_b32_e32 v38, v39, v38, vcc
	v_cmp_eq_u32_e32 vcc, 12, v173
	v_and_b32_e32 v39, 15, v59
	s_nop 0
	v_cndmask_b32_e32 v37, v38, v37, vcc
	v_cmp_eq_u32_e32 vcc, 13, v173
	s_nop 1
	v_cndmask_b32_e32 v36, v37, v36, vcc
	v_cmp_eq_u32_e32 vcc, 14, v173
	s_nop 1
	v_cndmask_b32_e32 v35, v36, v35, vcc
	v_cmp_eq_u32_e32 vcc, 15, v173
	v_exp_f32_e32 v36, v12
	v_and_b32_e32 v12, 0xffffff00, v32
	v_cndmask_b32_e32 v38, v35, v34, vcc
	v_cmp_eq_u32_e32 vcc, 0, v39
	v_sub_f32_e32 v12, v12, v60
	v_mul_f32_e32 v12, 0x3fb8aa3b, v12
	v_cndmask_b32_e32 v33, 0, v33, vcc
	v_cmp_eq_u32_e32 vcc, 1, v39
	v_exp_f32_e32 v37, v12
	s_nop 0
	v_cndmask_b32_e32 v17, v33, v17, vcc
	v_cmp_eq_u32_e32 vcc, 2, v39
	v_sub_f32_e32 v33, v51, v60
	v_mul_f32_e32 v33, 0x3fb8aa3b, v33
	v_cndmask_b32_e32 v17, v17, v18, vcc
	v_cmp_eq_u32_e32 vcc, 3, v39
	v_sub_f32_e32 v18, v60, v60
	v_mul_f32_e32 v18, 0x3fb8aa3b, v18
	v_cndmask_b32_e32 v17, v17, v19, vcc
	v_cmp_eq_u32_e32 vcc, 4, v39
	v_sub_f32_e32 v19, v61, v60
	v_exp_f32_e32 v18, v18
	v_cndmask_b32_e32 v17, v17, v20, vcc
	v_cmp_eq_u32_e32 vcc, 5, v39
	v_mul_f32_e32 v19, 0x3fb8aa3b, v19
	v_sub_f32_e32 v20, v62, v60
	v_cndmask_b32_e32 v17, v17, v21, vcc
	v_exp_f32_e32 v19, v19
	v_mul_f32_e32 v20, 0x3fb8aa3b, v20
	v_sub_f32_e32 v21, v63, v60
	v_cmp_eq_u32_e32 vcc, 6, v39
	v_exp_f32_e32 v20, v20
	v_mul_f32_e32 v21, 0x3fb8aa3b, v21
	v_cndmask_b32_e32 v17, v17, v22, vcc
	v_cmp_eq_u32_e32 vcc, 7, v39
	v_exp_f32_e32 v21, v21
	v_add_f32_e32 v22, 0, v18
	v_cndmask_b32_e32 v17, v17, v23, vcc
	v_cmp_eq_u32_e32 vcc, 8, v39
	v_add_f32_e32 v22, v19, v22
	v_add_f32_e32 v22, v20, v22
	v_cndmask_b32_e32 v17, v17, v24, vcc
	v_cmp_eq_u32_e32 vcc, 9, v39
	v_sub_f32_e32 v23, v56, v60
	v_mul_f32_e32 v23, 0x3fb8aa3b, v23
	v_cndmask_b32_e32 v17, v17, v25, vcc
	v_cmp_eq_u32_e32 vcc, 10, v39
	v_sub_f32_e32 v24, v55, v60
	v_exp_f32_e32 v23, v23
	v_cndmask_b32_e32 v17, v17, v26, vcc
	v_add_f32_e32 v26, v21, v22
	v_sub_f32_e32 v22, v58, v60
	v_mul_f32_e32 v22, 0x3fb8aa3b, v22
	v_exp_f32_e32 v22, v22
	v_mul_f32_e32 v24, 0x3fb8aa3b, v24
	v_sub_f32_e32 v25, v54, v60
	v_exp_f32_e32 v24, v24
	v_mul_f32_e32 v25, 0x3fb8aa3b, v25
	v_cmp_eq_u32_e32 vcc, 11, v39
	v_exp_f32_e32 v25, v25
	v_add_f32_e32 v26, v22, v26
	v_cndmask_b32_e32 v17, v17, v27, vcc
	v_cmp_eq_u32_e32 vcc, 12, v39
	v_add_f32_e32 v26, v23, v26
	v_add_f32_e32 v26, v24, v26
	v_cndmask_b32_e32 v17, v17, v28, vcc
	v_cmp_eq_u32_e32 vcc, 13, v39
	v_sub_f32_e32 v27, v57, v60
	v_mul_f32_e32 v27, 0x3fb8aa3b, v27
	v_cndmask_b32_e32 v17, v17, v29, vcc
	v_cmp_eq_u32_e32 vcc, 14, v39
	v_sub_f32_e32 v28, v53, v60
	v_exp_f32_e32 v27, v27
	v_cndmask_b32_e32 v17, v17, v30, vcc
	v_add_f32_e32 v30, v25, v26
	v_sub_f32_e32 v26, v209, v60
	v_mul_f32_e32 v26, 0x3fb8aa3b, v26
	v_exp_f32_e32 v26, v26
	v_mul_f32_e32 v28, 0x3fb8aa3b, v28
	v_sub_f32_e32 v29, v52, v60
	v_exp_f32_e32 v28, v28
	v_mul_f32_e32 v29, 0x3fb8aa3b, v29
	v_exp_f32_e32 v29, v29
	v_exp_f32_e32 v34, v33
	v_sub_f32_e32 v33, v50, v60
	v_add_f32_e32 v30, v26, v30
	v_mul_f32_e32 v33, 0x3fb8aa3b, v33
	v_add_f32_e32 v30, v27, v30
	v_exp_f32_e32 v35, v33
	v_add_f32_e32 v30, v28, v30
	v_add_f32_e32 v30, v29, v30
	v_add_f32_e32 v12, v34, v30
	v_add_f32_e32 v12, v35, v12
	v_add_f32_e32 v12, v36, v12
	v_add_f32_e32 v30, v37, v12
	v_div_scale_f32 v32, s[6:7], v30, v30, 1.0
	v_rcp_f32_e32 v33, v32
	v_cmp_eq_u32_e32 vcc, 15, v39
	v_readlane_b32 s6, v255, 46
	s_lshl_b32 s6, s6, 4
	v_cndmask_b32_e32 v12, v17, v31, vcc
	v_fma_f32 v17, -v32, v33, 1.0
	v_fmac_f32_e32 v33, v17, v33
	v_div_scale_f32 v17, vcc, 1.0, v30, 1.0
	v_mul_f32_e32 v31, v17, v33
	v_lshl_add_u32 v12, v38, 7, v12
	v_fma_f32 v38, -v32, v31, v17
	v_fmac_f32_e32 v31, v38, v33
	v_fma_f32 v17, -v32, v31, v17
	v_div_fmas_f32 v17, v17, v33, v31
	v_div_fixup_f32 v30, v17, v30, 1.0
	v_lshlrev_b64 v[16:17], 9, v[176:177]
	s_ashr_i32 s7, s6, 31
	v_lshl_add_u64 v[32:33], s[94:95], 0, v[16:17]
	s_lshl_b64 s[6:7], s[6:7], 2
	v_lshl_add_u64 v[32:33], v[32:33], 0, s[6:7]
	v_lshl_add_u64 v[16:17], s[8:9], 0, v[16:17]
	v_lshl_add_u64 v[16:17], v[16:17], 0, s[6:7]
	global_store_dwordx4 v[32:33], v[12:15], off
	v_readlane_b32 s8, v255, 44
	v_readlane_b32 s9, v255, 45
	v_pk_mul_f32 v[12:13], v[18:19], v[30:31] op_sel_hi:[1,0]
	v_pk_mul_f32 v[14:15], v[20:21], v[30:31] op_sel_hi:[1,0]
	global_store_dwordx4 v[16:17], v[12:15], off
	global_store_dwordx4 v[32:33], v[8:11], off offset:16
	s_nop 1
	v_pk_mul_f32 v[8:9], v[22:23], v[30:31] op_sel_hi:[1,0]
	v_pk_mul_f32 v[10:11], v[24:25], v[30:31] op_sel_hi:[1,0]
	global_store_dwordx4 v[16:17], v[8:11], off offset:16
	global_store_dwordx4 v[32:33], v[4:7], off offset:32
	s_nop 1
	v_pk_mul_f32 v[4:5], v[26:27], v[30:31] op_sel_hi:[1,0]
	v_pk_mul_f32 v[6:7], v[28:29], v[30:31] op_sel_hi:[1,0]
	global_store_dwordx4 v[16:17], v[4:7], off offset:32
	global_store_dwordx4 v[32:33], v[0:3], off offset:48
	s_nop 1
	v_pk_mul_f32 v[0:1], v[34:35], v[30:31] op_sel_hi:[1,0]
	v_pk_mul_f32 v[2:3], v[36:37], v[30:31] op_sel_hi:[1,0]
	global_store_dwordx4 v[16:17], v[0:3], off offset:48
	s_branch .LBB0_696
